# GEMM K-loops: loop-carried SALU (counter, pointer advance, exit test) moved in front of the trip's last barrier; only the branch stays behind it
# speedup vs baseline: 1.0138x; 1.0003x over previous
.Lrope_skip_ft:
	s_waitcnt vmcnt(8)
	s_waitcnt lgkmcnt(0)
	s_barrier
	s_setprio 1
	s_waitcnt lgkmcnt(7)
	v_mfma_f32_16x16x32_bf16 v[62:65], v[130:133], v[162:165], 0
	v_mfma_f32_16x16x32_bf16 v[58:61], v[134:137], v[162:165], 0
	s_waitcnt lgkmcnt(6)
	v_mfma_f32_16x16x32_bf16 v[54:57], v[130:133], v[166:169], 0
	v_mfma_f32_16x16x32_bf16 v[50:53], v[134:137], v[166:169], 0
	s_waitcnt lgkmcnt(3)
	v_mfma_f32_16x16x32_bf16 v[46:49], v[130:133], v[178:181], 0
	v_mfma_f32_16x16x32_bf16 v[42:45], v[134:137], v[178:181], 0
	s_waitcnt lgkmcnt(2)
	v_mfma_f32_16x16x32_bf16 v[38:41], v[130:133], v[182:185], 0
	v_mfma_f32_16x16x32_bf16 v[34:37], v[134:137], v[182:185], 0
	v_mfma_f32_16x16x32_bf16 v[62:65], v[138:141], v[170:173], v[62:65]
	v_mfma_f32_16x16x32_bf16 v[58:61], v[142:145], v[170:173], v[58:61]
	v_mfma_f32_16x16x32_bf16 v[54:57], v[138:141], v[174:177], v[54:57]
	v_mfma_f32_16x16x32_bf16 v[50:53], v[142:145], v[174:177], v[50:53]
	s_waitcnt lgkmcnt(1)
	v_mfma_f32_16x16x32_bf16 v[46:49], v[138:141], v[186:189], v[46:49]
	v_mfma_f32_16x16x32_bf16 v[42:45], v[142:145], v[186:189], v[42:45]
	s_waitcnt lgkmcnt(0)
	v_mfma_f32_16x16x32_bf16 v[38:41], v[138:141], v[190:193], v[38:41]
	v_mfma_f32_16x16x32_bf16 v[34:37], v[142:145], v[190:193], v[34:37]
	s_setprio 0
	s_setprio 1
	v_mfma_f32_16x16x32_bf16 v[30:33], v[146:149], v[162:165], 0
	v_mfma_f32_16x16x32_bf16 v[26:29], v[150:153], v[162:165], 0
	v_mfma_f32_16x16x32_bf16 v[22:25], v[146:149], v[166:169], 0
	v_mfma_f32_16x16x32_bf16 v[18:21], v[150:153], v[166:169], 0
	v_mfma_f32_16x16x32_bf16 v[14:17], v[146:149], v[178:181], 0
	v_mfma_f32_16x16x32_bf16 v[10:13], v[150:153], v[178:181], 0
	v_mfma_f32_16x16x32_bf16 v[6:9], v[146:149], v[182:185], 0
	v_mfma_f32_16x16x32_bf16 v[2:5], v[150:153], v[182:185], 0
	v_mfma_f32_16x16x32_bf16 v[30:33], v[154:157], v[170:173], v[30:33]
	v_mfma_f32_16x16x32_bf16 v[26:29], v[158:161], v[170:173], v[26:29]
	v_mfma_f32_16x16x32_bf16 v[22:25], v[154:157], v[174:177], v[22:25]
	v_mfma_f32_16x16x32_bf16 v[18:21], v[158:161], v[174:177], v[18:21]
	v_mfma_f32_16x16x32_bf16 v[14:17], v[154:157], v[186:189], v[14:17]
	v_mfma_f32_16x16x32_bf16 v[10:13], v[158:161], v[186:189], v[10:13]
	v_mfma_f32_16x16x32_bf16 v[6:9], v[154:157], v[190:193], v[6:9]
	v_mfma_f32_16x16x32_bf16 v[2:5], v[158:161], v[190:193], v[2:5]
	s_setprio 0
	s_barrier
	s_add_i32 s78, 0, 0x18000
	v_add_u32_e32 v162, s78, v217
	v_add_u32_e32 v163, s78, v218
	s_add_i32 s78, 0, 0x1c000
	v_add_u32_e32 v164, s78, v217
	ds_read_b128 v[130:133], v162
	ds_read_b128 v[134:137], v162 offset:2048
	ds_read_b128 v[138:141], v163
	ds_read_b128 v[142:145], v163 offset:2048
	v_add_u32_e32 v165, s78, v218
	ds_read_b128 v[146:149], v164
	ds_read_b128 v[150:153], v164 offset:2048
	ds_read_b128 v[154:157], v165
	ds_read_b128 v[158:161], v165 offset:2048
	ds_read_b128 v[166:169], v223 offset:32768
	ds_read_b128 v[170:173], v223 offset:34816
	ds_read_b128 v[174:177], v224 offset:32768
	ds_read_b128 v[178:181], v224 offset:34816
	ds_read_b128 v[182:185], v223 offset:36864
	ds_read_b128 v[186:189], v223 offset:38912
	ds_read_b128 v[190:193], v224 offset:36864
	ds_read_b128 v[198:201], v224 offset:38912
	s_mov_b32 m0, s62
	s_nop 0
	global_load_lds_dwordx4 v212, s[54:55] offset:0
	s_nop 0
	s_mov_b32 m0, s63
	s_nop 0
	global_load_lds_dwordx4 v214, s[54:55] offset:0
	s_waitcnt vmcnt(8)
	s_waitcnt lgkmcnt(0)
	s_barrier
	s_setprio 1
	s_waitcnt lgkmcnt(7)
	v_mfma_f32_16x16x32_bf16 v[126:129], v[130:133], v[166:169], v[126:129]
	v_mfma_f32_16x16x32_bf16 v[122:125], v[134:137], v[166:169], v[122:125]
	s_waitcnt lgkmcnt(6)
	v_mfma_f32_16x16x32_bf16 v[118:121], v[130:133], v[170:173], v[118:121]
	v_mfma_f32_16x16x32_bf16 v[114:117], v[134:137], v[170:173], v[114:117]
	s_waitcnt lgkmcnt(3)
	v_mfma_f32_16x16x32_bf16 v[110:113], v[130:133], v[182:185], v[110:113]
	v_mfma_f32_16x16x32_bf16 v[106:109], v[134:137], v[182:185], v[106:109]
	s_waitcnt lgkmcnt(2)
	v_mfma_f32_16x16x32_bf16 v[102:105], v[130:133], v[186:189], v[102:105]
	v_mfma_f32_16x16x32_bf16 v[98:101], v[134:137], v[186:189], v[98:101]
	v_mfma_f32_16x16x32_bf16 v[126:129], v[138:141], v[174:177], v[126:129]
	v_mfma_f32_16x16x32_bf16 v[122:125], v[142:145], v[174:177], v[122:125]
	v_mfma_f32_16x16x32_bf16 v[118:121], v[138:141], v[178:181], v[118:121]
	v_mfma_f32_16x16x32_bf16 v[114:117], v[142:145], v[178:181], v[114:117]
	s_waitcnt lgkmcnt(1)
	v_mfma_f32_16x16x32_bf16 v[110:113], v[138:141], v[190:193], v[110:113]
	v_mfma_f32_16x16x32_bf16 v[106:109], v[142:145], v[190:193], v[106:109]
	s_waitcnt lgkmcnt(0)
	v_mfma_f32_16x16x32_bf16 v[102:105], v[138:141], v[198:201], v[102:105]
	v_mfma_f32_16x16x32_bf16 v[98:101], v[142:145], v[198:201], v[98:101]
	s_setprio 0
	s_setprio 1
	v_mfma_f32_16x16x32_bf16 v[94:97], v[146:149], v[166:169], v[94:97]
	v_mfma_f32_16x16x32_bf16 v[90:93], v[150:153], v[166:169], v[90:93]
	v_mfma_f32_16x16x32_bf16 v[86:89], v[146:149], v[170:173], v[86:89]
	v_mfma_f32_16x16x32_bf16 v[82:85], v[150:153], v[170:173], v[82:85]
	v_mfma_f32_16x16x32_bf16 v[78:81], v[146:149], v[182:185], v[78:81]
	v_mfma_f32_16x16x32_bf16 v[74:77], v[150:153], v[182:185], v[74:77]
	v_mfma_f32_16x16x32_bf16 v[70:73], v[146:149], v[186:189], v[70:73]
	v_mfma_f32_16x16x32_bf16 v[66:69], v[150:153], v[186:189], v[66:69]
	v_mfma_f32_16x16x32_bf16 v[94:97], v[154:157], v[174:177], v[94:97]
	v_mfma_f32_16x16x32_bf16 v[90:93], v[158:161], v[174:177], v[90:93]
	v_mfma_f32_16x16x32_bf16 v[86:89], v[154:157], v[178:181], v[86:89]
	v_mfma_f32_16x16x32_bf16 v[82:85], v[158:161], v[178:181], v[82:85]
	v_mfma_f32_16x16x32_bf16 v[78:81], v[154:157], v[190:193], v[78:81]
	v_mfma_f32_16x16x32_bf16 v[74:77], v[158:161], v[190:193], v[74:77]
	v_mfma_f32_16x16x32_bf16 v[70:73], v[154:157], v[198:201], v[70:73]
	v_mfma_f32_16x16x32_bf16 v[66:69], v[158:161], v[198:201], v[66:69]
	s_setprio 0
	s_barrier
	ds_read_b128 v[166:169], v223 offset:49152
	ds_read_b128 v[170:173], v223 offset:51200
	ds_read_b128 v[174:177], v224 offset:49152
	ds_read_b128 v[178:181], v224 offset:51200
	ds_read_b128 v[182:185], v223 offset:53248
	ds_read_b128 v[186:189], v223 offset:55296
	ds_read_b128 v[190:193], v224 offset:53248
	ds_read_b128 v[198:201], v224 offset:55296
	s_add_u32 s54, s51, 0x180
	s_addc_u32 s55, s53, 0
	s_mov_b32 m0, s64
	s_nop 0
	global_load_lds_dwordx4 v215, s[54:55] offset:0
	s_nop 0
	s_mov_b32 m0, s65
	s_nop 0
	global_load_lds_dwordx4 v216, s[54:55] offset:0
	s_add_u32 s54, s51, 0x40180
	s_addc_u32 s55, s53, 0
	s_mov_b32 m0, s68
	s_nop 0
	global_load_lds_dwordx4 v215, s[54:55] offset:0
	s_nop 0
	s_mov_b32 m0, s69
	s_nop 0
	global_load_lds_dwordx4 v216, s[54:55] offset:0
	s_add_u32 s54, s47, 0x180
	s_addc_u32 s55, s50, 0
	s_mov_b32 m0, s66
	s_nop 0
	global_load_lds_dwordx4 v211, s[54:55] offset:0
	s_nop 0
	s_mov_b32 m0, s67
	s_nop 0
	global_load_lds_dwordx4 v213, s[54:55] offset:0
	s_waitcnt vmcnt(8)
	s_waitcnt lgkmcnt(0)
	s_barrier
	s_setprio 1
	s_waitcnt lgkmcnt(7)
	v_mfma_f32_16x16x32_bf16 v[62:65], v[130:133], v[166:169], v[62:65]
	v_mfma_f32_16x16x32_bf16 v[58:61], v[134:137], v[166:169], v[58:61]
	s_waitcnt lgkmcnt(6)
	v_mfma_f32_16x16x32_bf16 v[54:57], v[130:133], v[170:173], v[54:57]
	v_mfma_f32_16x16x32_bf16 v[50:53], v[134:137], v[170:173], v[50:53]
	s_waitcnt lgkmcnt(3)
	v_mfma_f32_16x16x32_bf16 v[46:49], v[130:133], v[182:185], v[46:49]
	v_mfma_f32_16x16x32_bf16 v[42:45], v[134:137], v[182:185], v[42:45]
	s_waitcnt lgkmcnt(2)
	v_mfma_f32_16x16x32_bf16 v[38:41], v[130:133], v[186:189], v[38:41]
	v_mfma_f32_16x16x32_bf16 v[34:37], v[134:137], v[186:189], v[34:37]
	v_mfma_f32_16x16x32_bf16 v[62:65], v[138:141], v[174:177], v[62:65]
	v_mfma_f32_16x16x32_bf16 v[58:61], v[142:145], v[174:177], v[58:61]
	v_mfma_f32_16x16x32_bf16 v[54:57], v[138:141], v[178:181], v[54:57]
	v_mfma_f32_16x16x32_bf16 v[50:53], v[142:145], v[178:181], v[50:53]
	s_waitcnt lgkmcnt(1)
	v_mfma_f32_16x16x32_bf16 v[46:49], v[138:141], v[190:193], v[46:49]
	v_mfma_f32_16x16x32_bf16 v[42:45], v[142:145], v[190:193], v[42:45]
	s_waitcnt lgkmcnt(0)
	v_mfma_f32_16x16x32_bf16 v[38:41], v[138:141], v[198:201], v[38:41]
	v_mfma_f32_16x16x32_bf16 v[34:37], v[142:145], v[198:201], v[34:37]
	s_setprio 0
	s_setprio 1
	v_mfma_f32_16x16x32_bf16 v[30:33], v[146:149], v[166:169], v[30:33]
	v_mfma_f32_16x16x32_bf16 v[26:29], v[150:153], v[166:169], v[26:29]
	v_mfma_f32_16x16x32_bf16 v[22:25], v[146:149], v[170:173], v[22:25]
	v_mfma_f32_16x16x32_bf16 v[18:21], v[150:153], v[170:173], v[18:21]
	v_mfma_f32_16x16x32_bf16 v[14:17], v[146:149], v[182:185], v[14:17]
	v_mfma_f32_16x16x32_bf16 v[10:13], v[150:153], v[182:185], v[10:13]
	v_mfma_f32_16x16x32_bf16 v[6:9], v[146:149], v[186:189], v[6:9]
	v_mfma_f32_16x16x32_bf16 v[2:5], v[150:153], v[186:189], v[2:5]
	v_mfma_f32_16x16x32_bf16 v[30:33], v[154:157], v[174:177], v[30:33]
	v_mfma_f32_16x16x32_bf16 v[26:29], v[158:161], v[174:177], v[26:29]
	v_mfma_f32_16x16x32_bf16 v[22:25], v[154:157], v[178:181], v[22:25]
	v_mfma_f32_16x16x32_bf16 v[18:21], v[158:161], v[178:181], v[18:21]
	v_mfma_f32_16x16x32_bf16 v[14:17], v[154:157], v[190:193], v[14:17]
	v_mfma_f32_16x16x32_bf16 v[10:13], v[158:161], v[190:193], v[10:13]
	v_mfma_f32_16x16x32_bf16 v[6:9], v[154:157], v[198:201], v[6:9]
	v_mfma_f32_16x16x32_bf16 v[2:5], v[158:161], v[198:201], v[2:5]
	s_setprio 0
	s_add_i32 s9, s9, 2
	s_add_u32 s4, s4, 0x100
	s_addc_u32 s5, s5, 0
	s_barrier

.Lrope_skip:
	s_waitcnt vmcnt(8)
	s_waitcnt lgkmcnt(0)
	s_barrier
	s_setprio 1
	s_waitcnt lgkmcnt(7)
	v_mfma_f32_16x16x32_bf16 v[62:65], v[130:133], v[162:165], v[62:65]
	v_mfma_f32_16x16x32_bf16 v[58:61], v[134:137], v[162:165], v[58:61]
	s_waitcnt lgkmcnt(6)
	v_mfma_f32_16x16x32_bf16 v[54:57], v[130:133], v[166:169], v[54:57]
	v_mfma_f32_16x16x32_bf16 v[50:53], v[134:137], v[166:169], v[50:53]
	s_waitcnt lgkmcnt(3)
	v_mfma_f32_16x16x32_bf16 v[46:49], v[130:133], v[178:181], v[46:49]
	v_mfma_f32_16x16x32_bf16 v[42:45], v[134:137], v[178:181], v[42:45]
	s_waitcnt lgkmcnt(2)
	v_mfma_f32_16x16x32_bf16 v[38:41], v[130:133], v[182:185], v[38:41]
	v_mfma_f32_16x16x32_bf16 v[34:37], v[134:137], v[182:185], v[34:37]
	v_mfma_f32_16x16x32_bf16 v[62:65], v[138:141], v[170:173], v[62:65]
	v_mfma_f32_16x16x32_bf16 v[58:61], v[142:145], v[170:173], v[58:61]
	v_mfma_f32_16x16x32_bf16 v[54:57], v[138:141], v[174:177], v[54:57]
	v_mfma_f32_16x16x32_bf16 v[50:53], v[142:145], v[174:177], v[50:53]
	s_waitcnt lgkmcnt(1)
	v_mfma_f32_16x16x32_bf16 v[46:49], v[138:141], v[186:189], v[46:49]
	v_mfma_f32_16x16x32_bf16 v[42:45], v[142:145], v[186:189], v[42:45]
	s_waitcnt lgkmcnt(0)
	v_mfma_f32_16x16x32_bf16 v[38:41], v[138:141], v[190:193], v[38:41]
	v_mfma_f32_16x16x32_bf16 v[34:37], v[142:145], v[190:193], v[34:37]
	s_setprio 0
	s_setprio 1
	v_mfma_f32_16x16x32_bf16 v[30:33], v[146:149], v[162:165], v[30:33]
	v_mfma_f32_16x16x32_bf16 v[26:29], v[150:153], v[162:165], v[26:29]
	v_mfma_f32_16x16x32_bf16 v[22:25], v[146:149], v[166:169], v[22:25]
	v_mfma_f32_16x16x32_bf16 v[18:21], v[150:153], v[166:169], v[18:21]
	v_mfma_f32_16x16x32_bf16 v[14:17], v[146:149], v[178:181], v[14:17]
	v_mfma_f32_16x16x32_bf16 v[10:13], v[150:153], v[178:181], v[10:13]
	v_mfma_f32_16x16x32_bf16 v[6:9], v[146:149], v[182:185], v[6:9]
	v_mfma_f32_16x16x32_bf16 v[2:5], v[150:153], v[182:185], v[2:5]
	v_mfma_f32_16x16x32_bf16 v[30:33], v[154:157], v[170:173], v[30:33]
	v_mfma_f32_16x16x32_bf16 v[26:29], v[158:161], v[170:173], v[26:29]
	v_mfma_f32_16x16x32_bf16 v[22:25], v[154:157], v[174:177], v[22:25]
	v_mfma_f32_16x16x32_bf16 v[18:21], v[158:161], v[174:177], v[18:21]
	v_mfma_f32_16x16x32_bf16 v[14:17], v[154:157], v[186:189], v[14:17]
	v_mfma_f32_16x16x32_bf16 v[10:13], v[158:161], v[186:189], v[10:13]
	v_mfma_f32_16x16x32_bf16 v[6:9], v[154:157], v[190:193], v[6:9]
	v_mfma_f32_16x16x32_bf16 v[2:5], v[158:161], v[190:193], v[2:5]
	s_setprio 0
	s_barrier
	s_add_i32 s78, 0, 0x18000
	v_add_u32_e32 v162, s78, v217
	v_add_u32_e32 v163, s78, v218
	s_add_i32 s78, 0, 0x1c000
	v_add_u32_e32 v164, s78, v217
	ds_read_b128 v[130:133], v162
	ds_read_b128 v[134:137], v162 offset:2048
	ds_read_b128 v[138:141], v163
	ds_read_b128 v[142:145], v163 offset:2048
	v_add_u32_e32 v165, s78, v218
	ds_read_b128 v[146:149], v164
	ds_read_b128 v[150:153], v164 offset:2048
	ds_read_b128 v[154:157], v165
	ds_read_b128 v[158:161], v165 offset:2048
	ds_read_b128 v[166:169], v223 offset:32768
	ds_read_b128 v[170:173], v223 offset:34816
	ds_read_b128 v[174:177], v224 offset:32768
	ds_read_b128 v[178:181], v224 offset:34816
	ds_read_b128 v[182:185], v223 offset:36864
	ds_read_b128 v[186:189], v223 offset:38912
	ds_read_b128 v[190:193], v224 offset:36864
	ds_read_b128 v[198:201], v224 offset:38912
	s_mov_b32 m0, s62
	s_nop 0
	global_load_lds_dwordx4 v212, s[54:55] offset:0
	s_nop 0
	s_mov_b32 m0, s63
	s_nop 0
	global_load_lds_dwordx4 v214, s[54:55] offset:0
	s_waitcnt vmcnt(8)
	s_waitcnt lgkmcnt(0)
	s_barrier
	s_setprio 1
	s_waitcnt lgkmcnt(7)
	v_mfma_f32_16x16x32_bf16 v[126:129], v[130:133], v[166:169], v[126:129]
	v_mfma_f32_16x16x32_bf16 v[122:125], v[134:137], v[166:169], v[122:125]
	s_waitcnt lgkmcnt(6)
	v_mfma_f32_16x16x32_bf16 v[118:121], v[130:133], v[170:173], v[118:121]
	v_mfma_f32_16x16x32_bf16 v[114:117], v[134:137], v[170:173], v[114:117]
	s_waitcnt lgkmcnt(3)
	v_mfma_f32_16x16x32_bf16 v[110:113], v[130:133], v[182:185], v[110:113]
	v_mfma_f32_16x16x32_bf16 v[106:109], v[134:137], v[182:185], v[106:109]
	s_waitcnt lgkmcnt(2)
	v_mfma_f32_16x16x32_bf16 v[102:105], v[130:133], v[186:189], v[102:105]
	v_mfma_f32_16x16x32_bf16 v[98:101], v[134:137], v[186:189], v[98:101]
	v_mfma_f32_16x16x32_bf16 v[126:129], v[138:141], v[174:177], v[126:129]
	v_mfma_f32_16x16x32_bf16 v[122:125], v[142:145], v[174:177], v[122:125]
	v_mfma_f32_16x16x32_bf16 v[118:121], v[138:141], v[178:181], v[118:121]
	v_mfma_f32_16x16x32_bf16 v[114:117], v[142:145], v[178:181], v[114:117]
	s_waitcnt lgkmcnt(1)
	v_mfma_f32_16x16x32_bf16 v[110:113], v[138:141], v[190:193], v[110:113]
	v_mfma_f32_16x16x32_bf16 v[106:109], v[142:145], v[190:193], v[106:109]
	s_waitcnt lgkmcnt(0)
	v_mfma_f32_16x16x32_bf16 v[102:105], v[138:141], v[198:201], v[102:105]
	v_mfma_f32_16x16x32_bf16 v[98:101], v[142:145], v[198:201], v[98:101]
	s_setprio 0
	s_setprio 1
	v_mfma_f32_16x16x32_bf16 v[94:97], v[146:149], v[166:169], v[94:97]
	v_mfma_f32_16x16x32_bf16 v[90:93], v[150:153], v[166:169], v[90:93]
	v_mfma_f32_16x16x32_bf16 v[86:89], v[146:149], v[170:173], v[86:89]
	v_mfma_f32_16x16x32_bf16 v[82:85], v[150:153], v[170:173], v[82:85]
	v_mfma_f32_16x16x32_bf16 v[78:81], v[146:149], v[182:185], v[78:81]
	v_mfma_f32_16x16x32_bf16 v[74:77], v[150:153], v[182:185], v[74:77]
	v_mfma_f32_16x16x32_bf16 v[70:73], v[146:149], v[186:189], v[70:73]
	v_mfma_f32_16x16x32_bf16 v[66:69], v[150:153], v[186:189], v[66:69]
	v_mfma_f32_16x16x32_bf16 v[94:97], v[154:157], v[174:177], v[94:97]
	v_mfma_f32_16x16x32_bf16 v[90:93], v[158:161], v[174:177], v[90:93]
	v_mfma_f32_16x16x32_bf16 v[86:89], v[154:157], v[178:181], v[86:89]
	v_mfma_f32_16x16x32_bf16 v[82:85], v[158:161], v[178:181], v[82:85]
	v_mfma_f32_16x16x32_bf16 v[78:81], v[154:157], v[190:193], v[78:81]
	v_mfma_f32_16x16x32_bf16 v[74:77], v[158:161], v[190:193], v[74:77]
	v_mfma_f32_16x16x32_bf16 v[70:73], v[154:157], v[198:201], v[70:73]
	v_mfma_f32_16x16x32_bf16 v[66:69], v[158:161], v[198:201], v[66:69]
	s_setprio 0
	s_barrier
	ds_read_b128 v[166:169], v223 offset:49152
	ds_read_b128 v[170:173], v223 offset:51200
	ds_read_b128 v[174:177], v224 offset:49152
	ds_read_b128 v[178:181], v224 offset:51200
	ds_read_b128 v[182:185], v223 offset:53248
	ds_read_b128 v[186:189], v223 offset:55296
	ds_read_b128 v[190:193], v224 offset:53248
	ds_read_b128 v[198:201], v224 offset:55296
	s_add_u32 s54, s51, 0x180
	s_addc_u32 s55, s53, 0
	s_mov_b32 m0, s64
	s_nop 0
	global_load_lds_dwordx4 v215, s[54:55] offset:0
	s_nop 0
	s_mov_b32 m0, s65
	s_nop 0
	global_load_lds_dwordx4 v216, s[54:55] offset:0
	s_add_u32 s54, s51, 0x40180
	s_addc_u32 s55, s53, 0
	s_mov_b32 m0, s68
	s_nop 0
	global_load_lds_dwordx4 v215, s[54:55] offset:0
	s_nop 0
	s_mov_b32 m0, s69
	s_nop 0
	global_load_lds_dwordx4 v216, s[54:55] offset:0
	s_add_u32 s54, s47, 0x180
	s_addc_u32 s55, s50, 0
	s_mov_b32 m0, s66
	s_nop 0
	global_load_lds_dwordx4 v211, s[54:55] offset:0
	s_nop 0
	s_mov_b32 m0, s67
	s_nop 0
	global_load_lds_dwordx4 v213, s[54:55] offset:0
	s_waitcnt vmcnt(8)
	s_waitcnt lgkmcnt(0)
	s_barrier
	s_setprio 1
	s_waitcnt lgkmcnt(7)
	v_mfma_f32_16x16x32_bf16 v[62:65], v[130:133], v[166:169], v[62:65]
	v_mfma_f32_16x16x32_bf16 v[58:61], v[134:137], v[166:169], v[58:61]
	s_waitcnt lgkmcnt(6)
	v_mfma_f32_16x16x32_bf16 v[54:57], v[130:133], v[170:173], v[54:57]
	v_mfma_f32_16x16x32_bf16 v[50:53], v[134:137], v[170:173], v[50:53]
	s_waitcnt lgkmcnt(3)
	v_mfma_f32_16x16x32_bf16 v[46:49], v[130:133], v[182:185], v[46:49]
	v_mfma_f32_16x16x32_bf16 v[42:45], v[134:137], v[182:185], v[42:45]
	s_waitcnt lgkmcnt(2)
	v_mfma_f32_16x16x32_bf16 v[38:41], v[130:133], v[186:189], v[38:41]
	v_mfma_f32_16x16x32_bf16 v[34:37], v[134:137], v[186:189], v[34:37]
	v_mfma_f32_16x16x32_bf16 v[62:65], v[138:141], v[174:177], v[62:65]
	v_mfma_f32_16x16x32_bf16 v[58:61], v[142:145], v[174:177], v[58:61]
	v_mfma_f32_16x16x32_bf16 v[54:57], v[138:141], v[178:181], v[54:57]
	v_mfma_f32_16x16x32_bf16 v[50:53], v[142:145], v[178:181], v[50:53]
	s_waitcnt lgkmcnt(1)
	v_mfma_f32_16x16x32_bf16 v[46:49], v[138:141], v[190:193], v[46:49]
	v_mfma_f32_16x16x32_bf16 v[42:45], v[142:145], v[190:193], v[42:45]
	s_waitcnt lgkmcnt(0)
	v_mfma_f32_16x16x32_bf16 v[38:41], v[138:141], v[198:201], v[38:41]
	v_mfma_f32_16x16x32_bf16 v[34:37], v[142:145], v[198:201], v[34:37]
	s_setprio 0
	s_setprio 1
	v_mfma_f32_16x16x32_bf16 v[30:33], v[146:149], v[166:169], v[30:33]
	v_mfma_f32_16x16x32_bf16 v[26:29], v[150:153], v[166:169], v[26:29]
	v_mfma_f32_16x16x32_bf16 v[22:25], v[146:149], v[170:173], v[22:25]
	v_mfma_f32_16x16x32_bf16 v[18:21], v[150:153], v[170:173], v[18:21]
	v_mfma_f32_16x16x32_bf16 v[14:17], v[146:149], v[182:185], v[14:17]
	v_mfma_f32_16x16x32_bf16 v[10:13], v[150:153], v[182:185], v[10:13]
	v_mfma_f32_16x16x32_bf16 v[6:9], v[146:149], v[186:189], v[6:9]
	v_mfma_f32_16x16x32_bf16 v[2:5], v[150:153], v[186:189], v[2:5]
	v_mfma_f32_16x16x32_bf16 v[30:33], v[154:157], v[174:177], v[30:33]
	v_mfma_f32_16x16x32_bf16 v[26:29], v[158:161], v[174:177], v[26:29]
	v_mfma_f32_16x16x32_bf16 v[22:25], v[154:157], v[178:181], v[22:25]
	v_mfma_f32_16x16x32_bf16 v[18:21], v[158:161], v[178:181], v[18:21]
	v_mfma_f32_16x16x32_bf16 v[14:17], v[154:157], v[190:193], v[14:17]
	v_mfma_f32_16x16x32_bf16 v[10:13], v[158:161], v[190:193], v[10:13]
	v_mfma_f32_16x16x32_bf16 v[6:9], v[154:157], v[198:201], v[6:9]
	v_mfma_f32_16x16x32_bf16 v[2:5], v[158:161], v[198:201], v[2:5]
	s_setprio 0
	s_add_i32 s9, s9, 2
	s_add_u32 s4, s4, 0x100
	s_addc_u32 s5, s5, 0
	s_cmp_lt_u32 s9, 12
	s_barrier
	s_cbranch_scc1 .LBB0_126
	ds_read_b128 v[146:149], v219
	ds_read_b128 v[150:153], v219 offset:2048
	ds_read_b128 v[158:161], v220
	ds_read_b128 v[154:157], v220 offset:2048
	ds_read_b128 v[130:133], v221
	ds_read_b128 v[134:137], v221 offset:2048
	ds_read_b128 v[142:145], v222
	ds_read_b128 v[138:141], v222 offset:2048
	ds_read_b128 v[166:169], v223
	ds_read_b128 v[170:173], v223 offset:2048
	ds_read_b128 v[174:177], v224
	ds_read_b128 v[178:181], v224 offset:2048
	ds_read_b128 v[182:185], v223 offset:4096
	ds_read_b128 v[186:189], v223 offset:6144
	ds_read_b128 v[190:193], v224 offset:4096
	ds_read_b128 v[198:201], v224 offset:6144
	s_mov_b32 m0, s70
	s_nop 0
	global_load_lds_dwordx4 v212, s[24:25] offset:0
	s_nop 0
	s_mov_b32 m0, s71
	s_nop 0
	global_load_lds_dwordx4 v214, s[24:25] offset:0
	s_waitcnt vmcnt(8)
	s_waitcnt lgkmcnt(0)
	s_barrier
	s_setprio 1
	s_waitcnt lgkmcnt(7)
	v_mfma_f32_16x16x32_bf16 v[126:129], v[146:149], v[166:169], v[126:129]
	v_mfma_f32_16x16x32_bf16 v[122:125], v[150:153], v[166:169], v[122:125]
	s_waitcnt lgkmcnt(6)
	v_mfma_f32_16x16x32_bf16 v[118:121], v[146:149], v[170:173], v[118:121]
	v_mfma_f32_16x16x32_bf16 v[114:117], v[150:153], v[170:173], v[114:117]
	s_waitcnt lgkmcnt(3)
	v_mfma_f32_16x16x32_bf16 v[110:113], v[146:149], v[182:185], v[110:113]
	v_mfma_f32_16x16x32_bf16 v[106:109], v[150:153], v[182:185], v[106:109]
	s_waitcnt lgkmcnt(2)
	v_mfma_f32_16x16x32_bf16 v[102:105], v[146:149], v[186:189], v[102:105]
	v_mfma_f32_16x16x32_bf16 v[98:101], v[150:153], v[186:189], v[98:101]
	v_mfma_f32_16x16x32_bf16 v[126:129], v[158:161], v[174:177], v[126:129]
	v_mfma_f32_16x16x32_bf16 v[122:125], v[154:157], v[174:177], v[122:125]
	v_mfma_f32_16x16x32_bf16 v[118:121], v[158:161], v[178:181], v[118:121]
	v_mfma_f32_16x16x32_bf16 v[114:117], v[154:157], v[178:181], v[114:117]
	s_waitcnt lgkmcnt(1)
	v_mfma_f32_16x16x32_bf16 v[110:113], v[158:161], v[190:193], v[110:113]
	v_mfma_f32_16x16x32_bf16 v[106:109], v[154:157], v[190:193], v[106:109]
	s_waitcnt lgkmcnt(0)
	v_mfma_f32_16x16x32_bf16 v[102:105], v[158:161], v[198:201], v[102:105]
	v_mfma_f32_16x16x32_bf16 v[98:101], v[154:157], v[198:201], v[98:101]
	s_setprio 0
	s_setprio 1
	v_mfma_f32_16x16x32_bf16 v[94:97], v[130:133], v[166:169], v[94:97]
	v_mfma_f32_16x16x32_bf16 v[90:93], v[134:137], v[166:169], v[90:93]
	v_mfma_f32_16x16x32_bf16 v[86:89], v[130:133], v[170:173], v[86:89]
	v_mfma_f32_16x16x32_bf16 v[82:85], v[134:137], v[170:173], v[82:85]
	v_mfma_f32_16x16x32_bf16 v[78:81], v[130:133], v[182:185], v[78:81]
	v_mfma_f32_16x16x32_bf16 v[74:77], v[134:137], v[182:185], v[74:77]
	v_mfma_f32_16x16x32_bf16 v[70:73], v[130:133], v[186:189], v[70:73]
	v_mfma_f32_16x16x32_bf16 v[66:69], v[134:137], v[186:189], v[66:69]
	v_mfma_f32_16x16x32_bf16 v[94:97], v[142:145], v[174:177], v[94:97]
	v_mfma_f32_16x16x32_bf16 v[90:93], v[138:141], v[174:177], v[90:93]
	v_mfma_f32_16x16x32_bf16 v[86:89], v[142:145], v[178:181], v[86:89]
	v_mfma_f32_16x16x32_bf16 v[82:85], v[138:141], v[178:181], v[82:85]
	v_mfma_f32_16x16x32_bf16 v[78:81], v[142:145], v[190:193], v[78:81]
	v_mfma_f32_16x16x32_bf16 v[74:77], v[138:141], v[190:193], v[74:77]
	v_mfma_f32_16x16x32_bf16 v[70:73], v[142:145], v[198:201], v[70:73]
	v_mfma_f32_16x16x32_bf16 v[66:69], v[138:141], v[198:201], v[66:69]
	s_setprio 0
	s_barrier
	v_cndmask_b32_e64 v166, 0, 1, s[6:7]
	v_cmp_ne_u32_e64 s[4:5], 1, v166
	s_andn2_b64 vcc, exec, s[6:7]
	s_cbranch_vccnz .LBB0_129
	v_mov_b32_e32 v166, v0
	s_nop 0
	v_lshlrev_b32_e32 v167, 4, v166
	v_bitop3_b32 v167, v167, s2, v166 bitop3:0x48
	v_lshlrev_b32_e32 v166, 8, v166
	v_lshl_or_b32 v167, s48, 19, v167
	v_and_b32_e32 v166, 0xfffff800, v166
	v_add_u32_e32 v211, v167, v166
	v_add_u32_e32 v212, 0x40000, v211
	v_add_u32_e32 v213, 0x20000, v211
	v_add_u32_e32 v214, 0x60000, v211

.LBB0_367:
	s_mov_b32 s31, -2
	s_mov_b64 s[6:7], 0
	.p2align 3
	s_nop 0
	ds_read_b128 v[130:133], v203
	ds_read_b128 v[134:137], v203 offset:2048
	ds_read_b128 v[138:141], v204
	ds_read_b128 v[142:145], v204 offset:2048
	ds_read_b128 v[146:149], v205
	ds_read_b128 v[150:153], v205 offset:2048
	ds_read_b128 v[154:157], v206
	ds_read_b128 v[158:161], v206 offset:2048
	ds_read_b128 v[162:165], v207
	ds_read_b128 v[166:169], v207 offset:2048
	ds_read_b128 v[174:177], v208
	ds_read_b128 v[178:181], v208 offset:2048
	ds_read_b128 v[182:185], v207 offset:4096
	ds_read_b128 v[210:213], v207 offset:6144
	ds_read_b128 v[214:217], v208 offset:4096
	ds_read_b128 v[218:221], v208 offset:6144
	s_add_u32 s36, s8, s6
	s_addc_u32 s37, s9, s7
	s_add_u32 s58, s36, 0x80
	s_addc_u32 s59, s37, 0
	s_mov_b32 m0, s52
	s_nop 0
	global_load_lds_dwordx4 v198, s[58:59] offset:0
	s_nop 0
	s_mov_b32 m0, s53
	s_nop 0
	global_load_lds_dwordx4 v200, s[58:59] offset:0
	s_waitcnt vmcnt(8)
	s_waitcnt lgkmcnt(0)
	s_barrier
	s_setprio 1
	s_waitcnt lgkmcnt(7)
	v_mfma_f32_16x16x32_bf16 v[126:129], v[130:133], v[162:165], 0
	v_mfma_f32_16x16x32_bf16 v[122:125], v[134:137], v[162:165], 0
	s_waitcnt lgkmcnt(6)
	v_mfma_f32_16x16x32_bf16 v[118:121], v[130:133], v[166:169], 0
	v_mfma_f32_16x16x32_bf16 v[114:117], v[134:137], v[166:169], 0
	s_waitcnt lgkmcnt(3)
	v_mfma_f32_16x16x32_bf16 v[110:113], v[130:133], v[182:185], 0
	v_mfma_f32_16x16x32_bf16 v[106:109], v[134:137], v[182:185], 0
	s_waitcnt lgkmcnt(2)
	v_mfma_f32_16x16x32_bf16 v[102:105], v[130:133], v[210:213], 0
	v_mfma_f32_16x16x32_bf16 v[98:101], v[134:137], v[210:213], 0
	v_mfma_f32_16x16x32_bf16 v[126:129], v[138:141], v[174:177], v[126:129]
	v_mfma_f32_16x16x32_bf16 v[122:125], v[142:145], v[174:177], v[122:125]
	v_mfma_f32_16x16x32_bf16 v[118:121], v[138:141], v[178:181], v[118:121]
	v_mfma_f32_16x16x32_bf16 v[114:117], v[142:145], v[178:181], v[114:117]
	s_waitcnt lgkmcnt(1)
	v_mfma_f32_16x16x32_bf16 v[110:113], v[138:141], v[214:217], v[110:113]
	v_mfma_f32_16x16x32_bf16 v[106:109], v[142:145], v[214:217], v[106:109]
	s_waitcnt lgkmcnt(0)
	v_mfma_f32_16x16x32_bf16 v[102:105], v[138:141], v[218:221], v[102:105]
	v_mfma_f32_16x16x32_bf16 v[98:101], v[142:145], v[218:221], v[98:101]
	s_setprio 0
	s_setprio 1
	v_mfma_f32_16x16x32_bf16 v[94:97], v[146:149], v[162:165], 0
	v_mfma_f32_16x16x32_bf16 v[90:93], v[150:153], v[162:165], 0
	v_mfma_f32_16x16x32_bf16 v[86:89], v[146:149], v[166:169], 0
	v_mfma_f32_16x16x32_bf16 v[82:85], v[150:153], v[166:169], 0
	v_mfma_f32_16x16x32_bf16 v[78:81], v[146:149], v[182:185], 0
	v_mfma_f32_16x16x32_bf16 v[74:77], v[150:153], v[182:185], 0
	v_mfma_f32_16x16x32_bf16 v[70:73], v[146:149], v[210:213], 0
	v_mfma_f32_16x16x32_bf16 v[66:69], v[150:153], v[210:213], 0
	v_mfma_f32_16x16x32_bf16 v[94:97], v[154:157], v[174:177], v[94:97]
	v_mfma_f32_16x16x32_bf16 v[90:93], v[158:161], v[174:177], v[90:93]
	v_mfma_f32_16x16x32_bf16 v[86:89], v[154:157], v[178:181], v[86:89]
	v_mfma_f32_16x16x32_bf16 v[82:85], v[158:161], v[178:181], v[82:85]
	v_mfma_f32_16x16x32_bf16 v[78:81], v[154:157], v[214:217], v[78:81]
	v_mfma_f32_16x16x32_bf16 v[74:77], v[158:161], v[214:217], v[74:77]
	v_mfma_f32_16x16x32_bf16 v[70:73], v[154:157], v[218:221], v[70:73]
	v_mfma_f32_16x16x32_bf16 v[66:69], v[158:161], v[218:221], v[66:69]
	s_setprio 0
	s_barrier
	s_add_u32 s60, s34, s6
	s_addc_u32 s61, s35, s7
	ds_read_b128 v[162:165], v207 offset:16384
	ds_read_b128 v[166:169], v207 offset:18432
	ds_read_b128 v[174:177], v208 offset:16384
	ds_read_b128 v[178:181], v208 offset:18432
	ds_read_b128 v[182:185], v207 offset:20480
	ds_read_b128 v[210:213], v207 offset:22528
	ds_read_b128 v[214:217], v208 offset:20480
	ds_read_b128 v[218:221], v208 offset:22528
	s_add_u32 s58, s60, 0x100
	s_addc_u32 s59, s61, 0
	s_mov_b32 m0, s39
	s_nop 0
	global_load_lds_dwordx4 v195, s[58:59] offset:0
	s_nop 0
	s_mov_b32 m0, s40
	s_nop 0
	global_load_lds_dwordx4 v196, s[58:59] offset:0
	s_add_u32 s58, s60, 0x40100
	s_addc_u32 s59, s61, 0
	s_mov_b32 m0, s41
	s_nop 0
	global_load_lds_dwordx4 v195, s[58:59] offset:0
	s_nop 0
	s_mov_b32 m0, s42
	s_nop 0
	global_load_lds_dwordx4 v196, s[58:59] offset:0
	s_add_u32 s58, s36, 0x100
	s_addc_u32 s59, s37, 0
	s_mov_b32 m0, s38
	s_nop 0
	global_load_lds_dwordx4 v197, s[58:59] offset:0
	s_nop 0
	s_mov_b32 m0, s43
	s_nop 0
	global_load_lds_dwordx4 v199, s[58:59] offset:0
	s_waitcnt vmcnt(8)
	s_waitcnt lgkmcnt(0)
	s_barrier
	s_setprio 1
	s_waitcnt lgkmcnt(7)
	v_mfma_f32_16x16x32_bf16 v[62:65], v[130:133], v[162:165], 0
	v_mfma_f32_16x16x32_bf16 v[58:61], v[134:137], v[162:165], 0
	s_waitcnt lgkmcnt(6)
	v_mfma_f32_16x16x32_bf16 v[54:57], v[130:133], v[166:169], 0
	v_mfma_f32_16x16x32_bf16 v[50:53], v[134:137], v[166:169], 0
	s_waitcnt lgkmcnt(3)
	v_mfma_f32_16x16x32_bf16 v[46:49], v[130:133], v[182:185], 0
	v_mfma_f32_16x16x32_bf16 v[42:45], v[134:137], v[182:185], 0
	s_waitcnt lgkmcnt(2)
	v_mfma_f32_16x16x32_bf16 v[38:41], v[130:133], v[210:213], 0
	v_mfma_f32_16x16x32_bf16 v[34:37], v[134:137], v[210:213], 0
	v_mfma_f32_16x16x32_bf16 v[62:65], v[138:141], v[174:177], v[62:65]
	v_mfma_f32_16x16x32_bf16 v[58:61], v[142:145], v[174:177], v[58:61]
	v_mfma_f32_16x16x32_bf16 v[54:57], v[138:141], v[178:181], v[54:57]
	v_mfma_f32_16x16x32_bf16 v[50:53], v[142:145], v[178:181], v[50:53]
	s_waitcnt lgkmcnt(1)
	v_mfma_f32_16x16x32_bf16 v[46:49], v[138:141], v[214:217], v[46:49]
	v_mfma_f32_16x16x32_bf16 v[42:45], v[142:145], v[214:217], v[42:45]
	s_waitcnt lgkmcnt(0)
	v_mfma_f32_16x16x32_bf16 v[38:41], v[138:141], v[218:221], v[38:41]
	v_mfma_f32_16x16x32_bf16 v[34:37], v[142:145], v[218:221], v[34:37]
	s_setprio 0
	s_setprio 1
	v_mfma_f32_16x16x32_bf16 v[30:33], v[146:149], v[162:165], 0
	v_mfma_f32_16x16x32_bf16 v[26:29], v[150:153], v[162:165], 0
	v_mfma_f32_16x16x32_bf16 v[22:25], v[146:149], v[166:169], 0
	v_mfma_f32_16x16x32_bf16 v[18:21], v[150:153], v[166:169], 0
	v_mfma_f32_16x16x32_bf16 v[14:17], v[146:149], v[182:185], 0
	v_mfma_f32_16x16x32_bf16 v[10:13], v[150:153], v[182:185], 0
	v_mfma_f32_16x16x32_bf16 v[6:9], v[146:149], v[210:213], 0
	v_mfma_f32_16x16x32_bf16 v[2:5], v[150:153], v[210:213], 0
	v_mfma_f32_16x16x32_bf16 v[30:33], v[154:157], v[174:177], v[30:33]
	v_mfma_f32_16x16x32_bf16 v[26:29], v[158:161], v[174:177], v[26:29]
	v_mfma_f32_16x16x32_bf16 v[22:25], v[154:157], v[178:181], v[22:25]
	v_mfma_f32_16x16x32_bf16 v[18:21], v[158:161], v[178:181], v[18:21]
	v_mfma_f32_16x16x32_bf16 v[14:17], v[154:157], v[214:217], v[14:17]
	v_mfma_f32_16x16x32_bf16 v[10:13], v[158:161], v[214:217], v[10:13]
	v_mfma_f32_16x16x32_bf16 v[6:9], v[154:157], v[218:221], v[6:9]
	v_mfma_f32_16x16x32_bf16 v[2:5], v[158:161], v[218:221], v[2:5]
	s_setprio 0
	s_barrier
	s_add_i32 s62, 0, 0x18000
	v_add_u32_e32 v174, s62, v201
	v_add_u32_e32 v175, s62, v202
	s_add_i32 s62, 0, 0x1c000
	v_add_u32_e32 v176, s62, v201
	ds_read_b128 v[130:133], v174
	ds_read_b128 v[134:137], v174 offset:2048
	ds_read_b128 v[138:141], v175
	ds_read_b128 v[142:145], v175 offset:2048
	v_add_u32_e32 v177, s62, v202
	ds_read_b128 v[146:149], v176
	ds_read_b128 v[150:153], v176 offset:2048
	ds_read_b128 v[154:157], v177
	ds_read_b128 v[158:161], v177 offset:2048
	ds_read_b128 v[162:165], v207 offset:32768
	ds_read_b128 v[166:169], v207 offset:34816
	ds_read_b128 v[178:181], v208 offset:32768
	ds_read_b128 v[182:185], v208 offset:34816
	ds_read_b128 v[210:213], v207 offset:36864
	ds_read_b128 v[214:217], v207 offset:38912
	ds_read_b128 v[218:221], v208 offset:36864
	ds_read_b128 v[222:225], v208 offset:38912
	s_mov_b32 m0, s44
	s_nop 0
	global_load_lds_dwordx4 v198, s[58:59] offset:0
	s_nop 0
	s_mov_b32 m0, s45
	s_nop 0
	global_load_lds_dwordx4 v200, s[58:59] offset:0
	s_waitcnt vmcnt(8)
	s_waitcnt lgkmcnt(0)
	s_barrier
	s_setprio 1
	s_waitcnt lgkmcnt(7)
	v_mfma_f32_16x16x32_bf16 v[126:129], v[130:133], v[162:165], v[126:129]
	v_mfma_f32_16x16x32_bf16 v[122:125], v[134:137], v[162:165], v[122:125]
	s_waitcnt lgkmcnt(6)
	v_mfma_f32_16x16x32_bf16 v[118:121], v[130:133], v[166:169], v[118:121]
	v_mfma_f32_16x16x32_bf16 v[114:117], v[134:137], v[166:169], v[114:117]
	s_waitcnt lgkmcnt(3)
	v_mfma_f32_16x16x32_bf16 v[110:113], v[130:133], v[210:213], v[110:113]
	v_mfma_f32_16x16x32_bf16 v[106:109], v[134:137], v[210:213], v[106:109]
	s_waitcnt lgkmcnt(2)
	v_mfma_f32_16x16x32_bf16 v[102:105], v[130:133], v[214:217], v[102:105]
	v_mfma_f32_16x16x32_bf16 v[98:101], v[134:137], v[214:217], v[98:101]
	v_mfma_f32_16x16x32_bf16 v[126:129], v[138:141], v[178:181], v[126:129]
	v_mfma_f32_16x16x32_bf16 v[122:125], v[142:145], v[178:181], v[122:125]
	v_mfma_f32_16x16x32_bf16 v[118:121], v[138:141], v[182:185], v[118:121]
	v_mfma_f32_16x16x32_bf16 v[114:117], v[142:145], v[182:185], v[114:117]
	s_waitcnt lgkmcnt(1)
	v_mfma_f32_16x16x32_bf16 v[110:113], v[138:141], v[218:221], v[110:113]
	v_mfma_f32_16x16x32_bf16 v[106:109], v[142:145], v[218:221], v[106:109]
	s_waitcnt lgkmcnt(0)
	v_mfma_f32_16x16x32_bf16 v[102:105], v[138:141], v[222:225], v[102:105]
	v_mfma_f32_16x16x32_bf16 v[98:101], v[142:145], v[222:225], v[98:101]
	s_setprio 0
	s_setprio 1
	v_mfma_f32_16x16x32_bf16 v[94:97], v[146:149], v[162:165], v[94:97]
	v_mfma_f32_16x16x32_bf16 v[90:93], v[150:153], v[162:165], v[90:93]
	v_mfma_f32_16x16x32_bf16 v[86:89], v[146:149], v[166:169], v[86:89]
	v_mfma_f32_16x16x32_bf16 v[82:85], v[150:153], v[166:169], v[82:85]
	v_mfma_f32_16x16x32_bf16 v[78:81], v[146:149], v[210:213], v[78:81]
	v_mfma_f32_16x16x32_bf16 v[74:77], v[150:153], v[210:213], v[74:77]
	v_mfma_f32_16x16x32_bf16 v[70:73], v[146:149], v[214:217], v[70:73]
	v_mfma_f32_16x16x32_bf16 v[66:69], v[150:153], v[214:217], v[66:69]
	v_mfma_f32_16x16x32_bf16 v[94:97], v[154:157], v[178:181], v[94:97]
	v_mfma_f32_16x16x32_bf16 v[90:93], v[158:161], v[178:181], v[90:93]
	v_mfma_f32_16x16x32_bf16 v[86:89], v[154:157], v[182:185], v[86:89]
	v_mfma_f32_16x16x32_bf16 v[82:85], v[158:161], v[182:185], v[82:85]
	v_mfma_f32_16x16x32_bf16 v[78:81], v[154:157], v[218:221], v[78:81]
	v_mfma_f32_16x16x32_bf16 v[74:77], v[158:161], v[218:221], v[74:77]
	v_mfma_f32_16x16x32_bf16 v[70:73], v[154:157], v[222:225], v[70:73]
	v_mfma_f32_16x16x32_bf16 v[66:69], v[158:161], v[222:225], v[66:69]
	s_setprio 0
	s_barrier
	ds_read_b128 v[162:165], v207 offset:49152
	ds_read_b128 v[166:169], v207 offset:51200
	ds_read_b128 v[178:181], v208 offset:49152
	ds_read_b128 v[182:185], v208 offset:51200
	ds_read_b128 v[210:213], v207 offset:53248
	ds_read_b128 v[214:217], v207 offset:55296
	ds_read_b128 v[218:221], v208 offset:53248
	ds_read_b128 v[222:225], v208 offset:55296
	s_add_u32 s58, s60, 0x180
	s_addc_u32 s59, s61, 0
	s_mov_b32 m0, s46
	s_nop 0
	global_load_lds_dwordx4 v195, s[58:59] offset:0
	s_nop 0
	s_mov_b32 m0, s47
	s_nop 0
	global_load_lds_dwordx4 v196, s[58:59] offset:0
	s_add_u32 s58, s60, 0x40180
	s_addc_u32 s59, s61, 0
	s_mov_b32 m0, s50
	s_nop 0
	global_load_lds_dwordx4 v195, s[58:59] offset:0
	s_add_u32 s36, s36, 0x180
	s_mov_b32 m0, s51
	s_nop 0
	global_load_lds_dwordx4 v196, s[58:59] offset:0
	s_addc_u32 s37, s37, 0
	s_mov_b32 m0, s48
	s_nop 0
	global_load_lds_dwordx4 v197, s[36:37] offset:0
	s_nop 0
	s_mov_b32 m0, s49
	s_nop 0
	global_load_lds_dwordx4 v199, s[36:37] offset:0
	s_waitcnt vmcnt(8)
	s_waitcnt lgkmcnt(0)
	s_barrier
	s_setprio 1
	s_waitcnt lgkmcnt(7)
	v_mfma_f32_16x16x32_bf16 v[62:65], v[130:133], v[162:165], v[62:65]
	v_mfma_f32_16x16x32_bf16 v[58:61], v[134:137], v[162:165], v[58:61]
	s_waitcnt lgkmcnt(6)
	v_mfma_f32_16x16x32_bf16 v[54:57], v[130:133], v[166:169], v[54:57]
	v_mfma_f32_16x16x32_bf16 v[50:53], v[134:137], v[166:169], v[50:53]
	s_waitcnt lgkmcnt(3)
	v_mfma_f32_16x16x32_bf16 v[46:49], v[130:133], v[210:213], v[46:49]
	v_mfma_f32_16x16x32_bf16 v[42:45], v[134:137], v[210:213], v[42:45]
	s_waitcnt lgkmcnt(2)
	v_mfma_f32_16x16x32_bf16 v[38:41], v[130:133], v[214:217], v[38:41]
	v_mfma_f32_16x16x32_bf16 v[34:37], v[134:137], v[214:217], v[34:37]
	v_mfma_f32_16x16x32_bf16 v[62:65], v[138:141], v[178:181], v[62:65]
	v_mfma_f32_16x16x32_bf16 v[58:61], v[142:145], v[178:181], v[58:61]
	v_mfma_f32_16x16x32_bf16 v[54:57], v[138:141], v[182:185], v[54:57]
	v_mfma_f32_16x16x32_bf16 v[50:53], v[142:145], v[182:185], v[50:53]
	s_waitcnt lgkmcnt(1)
	v_mfma_f32_16x16x32_bf16 v[46:49], v[138:141], v[218:221], v[46:49]
	v_mfma_f32_16x16x32_bf16 v[42:45], v[142:145], v[218:221], v[42:45]
	s_waitcnt lgkmcnt(0)
	v_mfma_f32_16x16x32_bf16 v[38:41], v[138:141], v[222:225], v[38:41]
	v_mfma_f32_16x16x32_bf16 v[34:37], v[142:145], v[222:225], v[34:37]
	s_setprio 0
	s_setprio 1
	v_mfma_f32_16x16x32_bf16 v[30:33], v[146:149], v[162:165], v[30:33]
	v_mfma_f32_16x16x32_bf16 v[26:29], v[150:153], v[162:165], v[26:29]
	v_mfma_f32_16x16x32_bf16 v[22:25], v[146:149], v[166:169], v[22:25]
	v_mfma_f32_16x16x32_bf16 v[18:21], v[150:153], v[166:169], v[18:21]
	v_mfma_f32_16x16x32_bf16 v[14:17], v[146:149], v[210:213], v[14:17]
	v_mfma_f32_16x16x32_bf16 v[10:13], v[150:153], v[210:213], v[10:13]
	v_mfma_f32_16x16x32_bf16 v[6:9], v[146:149], v[214:217], v[6:9]
	v_mfma_f32_16x16x32_bf16 v[2:5], v[150:153], v[214:217], v[2:5]
	v_mfma_f32_16x16x32_bf16 v[30:33], v[154:157], v[178:181], v[30:33]
	v_mfma_f32_16x16x32_bf16 v[26:29], v[158:161], v[178:181], v[26:29]
	v_mfma_f32_16x16x32_bf16 v[22:25], v[154:157], v[182:185], v[22:25]
	v_mfma_f32_16x16x32_bf16 v[18:21], v[158:161], v[182:185], v[18:21]
	v_mfma_f32_16x16x32_bf16 v[14:17], v[154:157], v[218:221], v[14:17]
	v_mfma_f32_16x16x32_bf16 v[10:13], v[158:161], v[218:221], v[10:13]
	v_mfma_f32_16x16x32_bf16 v[6:9], v[154:157], v[222:225], v[6:9]
	v_mfma_f32_16x16x32_bf16 v[2:5], v[158:161], v[222:225], v[2:5]
	s_setprio 0
	s_add_i32 s31, s31, 2
	s_add_u32 s6, s6, 0x100
	s_addc_u32 s7, s7, 0
	s_barrier
.LBB0_368:
	.p2align 3
	s_nop 0
	ds_read_b128 v[130:133], v203
	ds_read_b128 v[134:137], v203 offset:2048
	ds_read_b128 v[138:141], v204
	ds_read_b128 v[142:145], v204 offset:2048
	ds_read_b128 v[146:149], v205
	ds_read_b128 v[150:153], v205 offset:2048
	ds_read_b128 v[154:157], v206
	ds_read_b128 v[158:161], v206 offset:2048
	ds_read_b128 v[162:165], v207
	ds_read_b128 v[166:169], v207 offset:2048
	ds_read_b128 v[174:177], v208
	ds_read_b128 v[178:181], v208 offset:2048
	ds_read_b128 v[182:185], v207 offset:4096
	ds_read_b128 v[210:213], v207 offset:6144
	ds_read_b128 v[214:217], v208 offset:4096
	ds_read_b128 v[218:221], v208 offset:6144
	s_add_u32 s36, s8, s6
	s_addc_u32 s37, s9, s7
	s_add_u32 s58, s36, 0x80
	s_addc_u32 s59, s37, 0
	s_mov_b32 m0, s52
	s_nop 0
	global_load_lds_dwordx4 v198, s[58:59] offset:0
	s_nop 0
	s_mov_b32 m0, s53
	s_nop 0
	global_load_lds_dwordx4 v200, s[58:59] offset:0
	s_waitcnt vmcnt(8)
	s_waitcnt lgkmcnt(0)
	s_barrier
	s_setprio 1
	s_waitcnt lgkmcnt(7)
	v_mfma_f32_16x16x32_bf16 v[126:129], v[130:133], v[162:165], v[126:129]
	v_mfma_f32_16x16x32_bf16 v[122:125], v[134:137], v[162:165], v[122:125]
	s_waitcnt lgkmcnt(6)
	v_mfma_f32_16x16x32_bf16 v[118:121], v[130:133], v[166:169], v[118:121]
	v_mfma_f32_16x16x32_bf16 v[114:117], v[134:137], v[166:169], v[114:117]
	s_waitcnt lgkmcnt(3)
	v_mfma_f32_16x16x32_bf16 v[110:113], v[130:133], v[182:185], v[110:113]
	v_mfma_f32_16x16x32_bf16 v[106:109], v[134:137], v[182:185], v[106:109]
	s_waitcnt lgkmcnt(2)
	v_mfma_f32_16x16x32_bf16 v[102:105], v[130:133], v[210:213], v[102:105]
	v_mfma_f32_16x16x32_bf16 v[98:101], v[134:137], v[210:213], v[98:101]
	v_mfma_f32_16x16x32_bf16 v[126:129], v[138:141], v[174:177], v[126:129]
	v_mfma_f32_16x16x32_bf16 v[122:125], v[142:145], v[174:177], v[122:125]
	v_mfma_f32_16x16x32_bf16 v[118:121], v[138:141], v[178:181], v[118:121]
	v_mfma_f32_16x16x32_bf16 v[114:117], v[142:145], v[178:181], v[114:117]
	s_waitcnt lgkmcnt(1)
	v_mfma_f32_16x16x32_bf16 v[110:113], v[138:141], v[214:217], v[110:113]
	v_mfma_f32_16x16x32_bf16 v[106:109], v[142:145], v[214:217], v[106:109]
	s_waitcnt lgkmcnt(0)
	v_mfma_f32_16x16x32_bf16 v[102:105], v[138:141], v[218:221], v[102:105]
	v_mfma_f32_16x16x32_bf16 v[98:101], v[142:145], v[218:221], v[98:101]
	s_setprio 0
	s_setprio 1
	v_mfma_f32_16x16x32_bf16 v[94:97], v[146:149], v[162:165], v[94:97]
	v_mfma_f32_16x16x32_bf16 v[90:93], v[150:153], v[162:165], v[90:93]
	v_mfma_f32_16x16x32_bf16 v[86:89], v[146:149], v[166:169], v[86:89]
	v_mfma_f32_16x16x32_bf16 v[82:85], v[150:153], v[166:169], v[82:85]
	v_mfma_f32_16x16x32_bf16 v[78:81], v[146:149], v[182:185], v[78:81]
	v_mfma_f32_16x16x32_bf16 v[74:77], v[150:153], v[182:185], v[74:77]
	v_mfma_f32_16x16x32_bf16 v[70:73], v[146:149], v[210:213], v[70:73]
	v_mfma_f32_16x16x32_bf16 v[66:69], v[150:153], v[210:213], v[66:69]
	v_mfma_f32_16x16x32_bf16 v[94:97], v[154:157], v[174:177], v[94:97]
	v_mfma_f32_16x16x32_bf16 v[90:93], v[158:161], v[174:177], v[90:93]
	v_mfma_f32_16x16x32_bf16 v[86:89], v[154:157], v[178:181], v[86:89]
	v_mfma_f32_16x16x32_bf16 v[82:85], v[158:161], v[178:181], v[82:85]
	v_mfma_f32_16x16x32_bf16 v[78:81], v[154:157], v[214:217], v[78:81]
	v_mfma_f32_16x16x32_bf16 v[74:77], v[158:161], v[214:217], v[74:77]
	v_mfma_f32_16x16x32_bf16 v[70:73], v[154:157], v[218:221], v[70:73]
	v_mfma_f32_16x16x32_bf16 v[66:69], v[158:161], v[218:221], v[66:69]
	s_setprio 0
	s_barrier
	s_add_u32 s60, s34, s6
	s_addc_u32 s61, s35, s7
	ds_read_b128 v[162:165], v207 offset:16384
	ds_read_b128 v[166:169], v207 offset:18432
	ds_read_b128 v[174:177], v208 offset:16384
	ds_read_b128 v[178:181], v208 offset:18432
	ds_read_b128 v[182:185], v207 offset:20480
	ds_read_b128 v[210:213], v207 offset:22528
	ds_read_b128 v[214:217], v208 offset:20480
	ds_read_b128 v[218:221], v208 offset:22528
	s_add_u32 s58, s60, 0x100
	s_addc_u32 s59, s61, 0
	s_mov_b32 m0, s39
	s_nop 0
	global_load_lds_dwordx4 v195, s[58:59] offset:0
	s_nop 0
	s_mov_b32 m0, s40
	s_nop 0
	global_load_lds_dwordx4 v196, s[58:59] offset:0
	s_add_u32 s58, s60, 0x40100
	s_addc_u32 s59, s61, 0
	s_mov_b32 m0, s41
	s_nop 0
	global_load_lds_dwordx4 v195, s[58:59] offset:0
	s_nop 0
	s_mov_b32 m0, s42
	s_nop 0
	global_load_lds_dwordx4 v196, s[58:59] offset:0
	s_add_u32 s58, s36, 0x100
	s_addc_u32 s59, s37, 0
	s_mov_b32 m0, s38
	s_nop 0
	global_load_lds_dwordx4 v197, s[58:59] offset:0
	s_nop 0
	s_mov_b32 m0, s43
	s_nop 0
	global_load_lds_dwordx4 v199, s[58:59] offset:0
	s_waitcnt vmcnt(8)
	s_waitcnt lgkmcnt(0)
	s_barrier
	s_setprio 1
	s_waitcnt lgkmcnt(7)
	v_mfma_f32_16x16x32_bf16 v[62:65], v[130:133], v[162:165], v[62:65]
	v_mfma_f32_16x16x32_bf16 v[58:61], v[134:137], v[162:165], v[58:61]
	s_waitcnt lgkmcnt(6)
	v_mfma_f32_16x16x32_bf16 v[54:57], v[130:133], v[166:169], v[54:57]
	v_mfma_f32_16x16x32_bf16 v[50:53], v[134:137], v[166:169], v[50:53]
	s_waitcnt lgkmcnt(3)
	v_mfma_f32_16x16x32_bf16 v[46:49], v[130:133], v[182:185], v[46:49]
	v_mfma_f32_16x16x32_bf16 v[42:45], v[134:137], v[182:185], v[42:45]
	s_waitcnt lgkmcnt(2)
	v_mfma_f32_16x16x32_bf16 v[38:41], v[130:133], v[210:213], v[38:41]
	v_mfma_f32_16x16x32_bf16 v[34:37], v[134:137], v[210:213], v[34:37]
	v_mfma_f32_16x16x32_bf16 v[62:65], v[138:141], v[174:177], v[62:65]
	v_mfma_f32_16x16x32_bf16 v[58:61], v[142:145], v[174:177], v[58:61]
	v_mfma_f32_16x16x32_bf16 v[54:57], v[138:141], v[178:181], v[54:57]
	v_mfma_f32_16x16x32_bf16 v[50:53], v[142:145], v[178:181], v[50:53]
	s_waitcnt lgkmcnt(1)
	v_mfma_f32_16x16x32_bf16 v[46:49], v[138:141], v[214:217], v[46:49]
	v_mfma_f32_16x16x32_bf16 v[42:45], v[142:145], v[214:217], v[42:45]
	s_waitcnt lgkmcnt(0)
	v_mfma_f32_16x16x32_bf16 v[38:41], v[138:141], v[218:221], v[38:41]
	v_mfma_f32_16x16x32_bf16 v[34:37], v[142:145], v[218:221], v[34:37]
	s_setprio 0
	s_setprio 1
	v_mfma_f32_16x16x32_bf16 v[30:33], v[146:149], v[162:165], v[30:33]
	v_mfma_f32_16x16x32_bf16 v[26:29], v[150:153], v[162:165], v[26:29]
	v_mfma_f32_16x16x32_bf16 v[22:25], v[146:149], v[166:169], v[22:25]
	v_mfma_f32_16x16x32_bf16 v[18:21], v[150:153], v[166:169], v[18:21]
	v_mfma_f32_16x16x32_bf16 v[14:17], v[146:149], v[182:185], v[14:17]
	v_mfma_f32_16x16x32_bf16 v[10:13], v[150:153], v[182:185], v[10:13]
	v_mfma_f32_16x16x32_bf16 v[6:9], v[146:149], v[210:213], v[6:9]
	v_mfma_f32_16x16x32_bf16 v[2:5], v[150:153], v[210:213], v[2:5]
	v_mfma_f32_16x16x32_bf16 v[30:33], v[154:157], v[174:177], v[30:33]
	v_mfma_f32_16x16x32_bf16 v[26:29], v[158:161], v[174:177], v[26:29]
	v_mfma_f32_16x16x32_bf16 v[22:25], v[154:157], v[178:181], v[22:25]
	v_mfma_f32_16x16x32_bf16 v[18:21], v[158:161], v[178:181], v[18:21]
	v_mfma_f32_16x16x32_bf16 v[14:17], v[154:157], v[214:217], v[14:17]
	v_mfma_f32_16x16x32_bf16 v[10:13], v[158:161], v[214:217], v[10:13]
	v_mfma_f32_16x16x32_bf16 v[6:9], v[154:157], v[218:221], v[6:9]
	v_mfma_f32_16x16x32_bf16 v[2:5], v[158:161], v[218:221], v[2:5]
	s_setprio 0
	s_barrier
	s_add_i32 s62, 0, 0x18000
	v_add_u32_e32 v174, s62, v201
	v_add_u32_e32 v175, s62, v202
	s_add_i32 s62, 0, 0x1c000
	v_add_u32_e32 v176, s62, v201
	ds_read_b128 v[130:133], v174
	ds_read_b128 v[134:137], v174 offset:2048
	ds_read_b128 v[138:141], v175
	ds_read_b128 v[142:145], v175 offset:2048
	v_add_u32_e32 v177, s62, v202
	ds_read_b128 v[146:149], v176
	ds_read_b128 v[150:153], v176 offset:2048
	ds_read_b128 v[154:157], v177
	ds_read_b128 v[158:161], v177 offset:2048
	ds_read_b128 v[162:165], v207 offset:32768
	ds_read_b128 v[166:169], v207 offset:34816
	ds_read_b128 v[178:181], v208 offset:32768
	ds_read_b128 v[182:185], v208 offset:34816
	ds_read_b128 v[210:213], v207 offset:36864
	ds_read_b128 v[214:217], v207 offset:38912
	ds_read_b128 v[218:221], v208 offset:36864
	ds_read_b128 v[222:225], v208 offset:38912
	s_mov_b32 m0, s44
	s_nop 0
	global_load_lds_dwordx4 v198, s[58:59] offset:0
	s_nop 0
	s_mov_b32 m0, s45
	s_nop 0
	global_load_lds_dwordx4 v200, s[58:59] offset:0
	s_waitcnt vmcnt(8)
	s_waitcnt lgkmcnt(0)
	s_barrier
	s_setprio 1
	s_waitcnt lgkmcnt(7)
	v_mfma_f32_16x16x32_bf16 v[126:129], v[130:133], v[162:165], v[126:129]
	v_mfma_f32_16x16x32_bf16 v[122:125], v[134:137], v[162:165], v[122:125]
	s_waitcnt lgkmcnt(6)
	v_mfma_f32_16x16x32_bf16 v[118:121], v[130:133], v[166:169], v[118:121]
	v_mfma_f32_16x16x32_bf16 v[114:117], v[134:137], v[166:169], v[114:117]
	s_waitcnt lgkmcnt(3)
	v_mfma_f32_16x16x32_bf16 v[110:113], v[130:133], v[210:213], v[110:113]
	v_mfma_f32_16x16x32_bf16 v[106:109], v[134:137], v[210:213], v[106:109]
	s_waitcnt lgkmcnt(2)
	v_mfma_f32_16x16x32_bf16 v[102:105], v[130:133], v[214:217], v[102:105]
	v_mfma_f32_16x16x32_bf16 v[98:101], v[134:137], v[214:217], v[98:101]
	v_mfma_f32_16x16x32_bf16 v[126:129], v[138:141], v[178:181], v[126:129]
	v_mfma_f32_16x16x32_bf16 v[122:125], v[142:145], v[178:181], v[122:125]
	v_mfma_f32_16x16x32_bf16 v[118:121], v[138:141], v[182:185], v[118:121]
	v_mfma_f32_16x16x32_bf16 v[114:117], v[142:145], v[182:185], v[114:117]
	s_waitcnt lgkmcnt(1)
	v_mfma_f32_16x16x32_bf16 v[110:113], v[138:141], v[218:221], v[110:113]
	v_mfma_f32_16x16x32_bf16 v[106:109], v[142:145], v[218:221], v[106:109]
	s_waitcnt lgkmcnt(0)
	v_mfma_f32_16x16x32_bf16 v[102:105], v[138:141], v[222:225], v[102:105]
	v_mfma_f32_16x16x32_bf16 v[98:101], v[142:145], v[222:225], v[98:101]
	s_setprio 0
	s_setprio 1
	v_mfma_f32_16x16x32_bf16 v[94:97], v[146:149], v[162:165], v[94:97]
	v_mfma_f32_16x16x32_bf16 v[90:93], v[150:153], v[162:165], v[90:93]
	v_mfma_f32_16x16x32_bf16 v[86:89], v[146:149], v[166:169], v[86:89]
	v_mfma_f32_16x16x32_bf16 v[82:85], v[150:153], v[166:169], v[82:85]
	v_mfma_f32_16x16x32_bf16 v[78:81], v[146:149], v[210:213], v[78:81]
	v_mfma_f32_16x16x32_bf16 v[74:77], v[150:153], v[210:213], v[74:77]
	v_mfma_f32_16x16x32_bf16 v[70:73], v[146:149], v[214:217], v[70:73]
	v_mfma_f32_16x16x32_bf16 v[66:69], v[150:153], v[214:217], v[66:69]
	v_mfma_f32_16x16x32_bf16 v[94:97], v[154:157], v[178:181], v[94:97]
	v_mfma_f32_16x16x32_bf16 v[90:93], v[158:161], v[178:181], v[90:93]
	v_mfma_f32_16x16x32_bf16 v[86:89], v[154:157], v[182:185], v[86:89]
	v_mfma_f32_16x16x32_bf16 v[82:85], v[158:161], v[182:185], v[82:85]
	v_mfma_f32_16x16x32_bf16 v[78:81], v[154:157], v[218:221], v[78:81]
	v_mfma_f32_16x16x32_bf16 v[74:77], v[158:161], v[218:221], v[74:77]
	v_mfma_f32_16x16x32_bf16 v[70:73], v[154:157], v[222:225], v[70:73]
	v_mfma_f32_16x16x32_bf16 v[66:69], v[158:161], v[222:225], v[66:69]
	s_setprio 0
	s_barrier
	ds_read_b128 v[162:165], v207 offset:49152
	ds_read_b128 v[166:169], v207 offset:51200
	ds_read_b128 v[178:181], v208 offset:49152
	ds_read_b128 v[182:185], v208 offset:51200
	ds_read_b128 v[210:213], v207 offset:53248
	ds_read_b128 v[214:217], v207 offset:55296
	ds_read_b128 v[218:221], v208 offset:53248
	ds_read_b128 v[222:225], v208 offset:55296
	s_add_u32 s58, s60, 0x180
	s_addc_u32 s59, s61, 0
	s_mov_b32 m0, s46
	s_nop 0
	global_load_lds_dwordx4 v195, s[58:59] offset:0
	s_nop 0
	s_mov_b32 m0, s47
	s_nop 0
	global_load_lds_dwordx4 v196, s[58:59] offset:0
	s_add_u32 s58, s60, 0x40180
	s_addc_u32 s59, s61, 0
	s_mov_b32 m0, s50
	s_nop 0
	global_load_lds_dwordx4 v195, s[58:59] offset:0
	s_add_u32 s36, s36, 0x180
	s_mov_b32 m0, s51
	s_nop 0
	global_load_lds_dwordx4 v196, s[58:59] offset:0
	s_addc_u32 s37, s37, 0
	s_mov_b32 m0, s48
	s_nop 0
	global_load_lds_dwordx4 v197, s[36:37] offset:0
	s_nop 0
	s_mov_b32 m0, s49
	s_nop 0
	global_load_lds_dwordx4 v199, s[36:37] offset:0
	s_waitcnt vmcnt(8)
	s_waitcnt lgkmcnt(0)
	s_barrier
	s_setprio 1
	s_waitcnt lgkmcnt(7)
	v_mfma_f32_16x16x32_bf16 v[62:65], v[130:133], v[162:165], v[62:65]
	v_mfma_f32_16x16x32_bf16 v[58:61], v[134:137], v[162:165], v[58:61]
	s_waitcnt lgkmcnt(6)
	v_mfma_f32_16x16x32_bf16 v[54:57], v[130:133], v[166:169], v[54:57]
	v_mfma_f32_16x16x32_bf16 v[50:53], v[134:137], v[166:169], v[50:53]
	s_waitcnt lgkmcnt(3)
	v_mfma_f32_16x16x32_bf16 v[46:49], v[130:133], v[210:213], v[46:49]
	v_mfma_f32_16x16x32_bf16 v[42:45], v[134:137], v[210:213], v[42:45]
	s_waitcnt lgkmcnt(2)
	v_mfma_f32_16x16x32_bf16 v[38:41], v[130:133], v[214:217], v[38:41]
	v_mfma_f32_16x16x32_bf16 v[34:37], v[134:137], v[214:217], v[34:37]
	v_mfma_f32_16x16x32_bf16 v[62:65], v[138:141], v[178:181], v[62:65]
	v_mfma_f32_16x16x32_bf16 v[58:61], v[142:145], v[178:181], v[58:61]
	v_mfma_f32_16x16x32_bf16 v[54:57], v[138:141], v[182:185], v[54:57]
	v_mfma_f32_16x16x32_bf16 v[50:53], v[142:145], v[182:185], v[50:53]
	s_waitcnt lgkmcnt(1)
	v_mfma_f32_16x16x32_bf16 v[46:49], v[138:141], v[218:221], v[46:49]
	v_mfma_f32_16x16x32_bf16 v[42:45], v[142:145], v[218:221], v[42:45]
	s_waitcnt lgkmcnt(0)
	v_mfma_f32_16x16x32_bf16 v[38:41], v[138:141], v[222:225], v[38:41]
	v_mfma_f32_16x16x32_bf16 v[34:37], v[142:145], v[222:225], v[34:37]
	s_setprio 0
	s_setprio 1
	v_mfma_f32_16x16x32_bf16 v[30:33], v[146:149], v[162:165], v[30:33]
	v_mfma_f32_16x16x32_bf16 v[26:29], v[150:153], v[162:165], v[26:29]
	v_mfma_f32_16x16x32_bf16 v[22:25], v[146:149], v[166:169], v[22:25]
	v_mfma_f32_16x16x32_bf16 v[18:21], v[150:153], v[166:169], v[18:21]
	v_mfma_f32_16x16x32_bf16 v[14:17], v[146:149], v[210:213], v[14:17]
	v_mfma_f32_16x16x32_bf16 v[10:13], v[150:153], v[210:213], v[10:13]
	v_mfma_f32_16x16x32_bf16 v[6:9], v[146:149], v[214:217], v[6:9]
	v_mfma_f32_16x16x32_bf16 v[2:5], v[150:153], v[214:217], v[2:5]
	v_mfma_f32_16x16x32_bf16 v[30:33], v[154:157], v[178:181], v[30:33]
	v_mfma_f32_16x16x32_bf16 v[26:29], v[158:161], v[178:181], v[26:29]
	v_mfma_f32_16x16x32_bf16 v[22:25], v[154:157], v[182:185], v[22:25]
	v_mfma_f32_16x16x32_bf16 v[18:21], v[158:161], v[182:185], v[18:21]
	v_mfma_f32_16x16x32_bf16 v[14:17], v[154:157], v[218:221], v[14:17]
	v_mfma_f32_16x16x32_bf16 v[10:13], v[158:161], v[218:221], v[10:13]
	v_mfma_f32_16x16x32_bf16 v[6:9], v[154:157], v[222:225], v[6:9]
	v_mfma_f32_16x16x32_bf16 v[2:5], v[158:161], v[222:225], v[2:5]
	s_setprio 0
	s_add_i32 s31, s31, 2
	s_add_u32 s6, s6, 0x100
	s_addc_u32 s7, s7, 0
	s_cmp_lt_u32 s31, 12
	s_barrier
	s_cbranch_scc1 .LBB0_368
	ds_read_b128 v[154:157], v203
	ds_read_b128 v[158:161], v203 offset:2048
	ds_read_b128 v[166:169], v204
	ds_read_b128 v[162:165], v204 offset:2048
	ds_read_b128 v[138:141], v205
	ds_read_b128 v[142:145], v205 offset:2048
	ds_read_b128 v[150:153], v206
	ds_read_b128 v[146:149], v206 offset:2048
	ds_read_b128 v[134:137], v207
	ds_read_b128 v[178:181], v207 offset:2048
	ds_read_b128 v[182:185], v208
	ds_read_b128 v[210:213], v208 offset:2048
	ds_read_b128 v[214:217], v207 offset:4096
	ds_read_b128 v[218:221], v207 offset:6144
	ds_read_b128 v[222:225], v208 offset:4096
	ds_read_b128 v[226:229], v208 offset:6144
	s_mov_b32 m0, s52
	s_nop 0
	global_load_lds_dwordx4 v198, s[20:21] offset:0
	s_nop 0
	s_mov_b32 m0, s53
	s_nop 0
	global_load_lds_dwordx4 v200, s[20:21] offset:0
	s_waitcnt vmcnt(8)
	s_waitcnt lgkmcnt(0)
	s_barrier
	s_setprio 1
	s_waitcnt lgkmcnt(7)
	v_mfma_f32_16x16x32_bf16 v[126:129], v[154:157], v[134:137], v[126:129]
	v_mfma_f32_16x16x32_bf16 v[122:125], v[158:161], v[134:137], v[122:125]
	s_waitcnt lgkmcnt(6)
	v_mfma_f32_16x16x32_bf16 v[118:121], v[154:157], v[178:181], v[118:121]
	v_mfma_f32_16x16x32_bf16 v[114:117], v[158:161], v[178:181], v[114:117]
	s_waitcnt lgkmcnt(3)
	v_mfma_f32_16x16x32_bf16 v[110:113], v[154:157], v[214:217], v[110:113]
	v_mfma_f32_16x16x32_bf16 v[106:109], v[158:161], v[214:217], v[106:109]
	s_waitcnt lgkmcnt(2)
	v_mfma_f32_16x16x32_bf16 v[102:105], v[154:157], v[218:221], v[102:105]
	v_mfma_f32_16x16x32_bf16 v[98:101], v[158:161], v[218:221], v[98:101]
	v_mfma_f32_16x16x32_bf16 v[126:129], v[166:169], v[182:185], v[126:129]
	v_mfma_f32_16x16x32_bf16 v[122:125], v[162:165], v[182:185], v[122:125]
	v_mfma_f32_16x16x32_bf16 v[118:121], v[166:169], v[210:213], v[118:121]
	v_mfma_f32_16x16x32_bf16 v[114:117], v[162:165], v[210:213], v[114:117]
	s_waitcnt lgkmcnt(1)
	v_mfma_f32_16x16x32_bf16 v[110:113], v[166:169], v[222:225], v[110:113]
	v_mfma_f32_16x16x32_bf16 v[106:109], v[162:165], v[222:225], v[106:109]
	s_waitcnt lgkmcnt(0)
	v_mfma_f32_16x16x32_bf16 v[102:105], v[166:169], v[226:229], v[102:105]
	v_mfma_f32_16x16x32_bf16 v[98:101], v[162:165], v[226:229], v[98:101]
	s_setprio 0
	s_setprio 1
	v_mfma_f32_16x16x32_bf16 v[94:97], v[138:141], v[134:137], v[94:97]
	v_mfma_f32_16x16x32_bf16 v[90:93], v[142:145], v[134:137], v[90:93]
	v_mfma_f32_16x16x32_bf16 v[86:89], v[138:141], v[178:181], v[86:89]
	v_mfma_f32_16x16x32_bf16 v[82:85], v[142:145], v[178:181], v[82:85]
	v_mfma_f32_16x16x32_bf16 v[78:81], v[138:141], v[214:217], v[78:81]
	v_mfma_f32_16x16x32_bf16 v[74:77], v[142:145], v[214:217], v[74:77]
	v_mfma_f32_16x16x32_bf16 v[70:73], v[138:141], v[218:221], v[70:73]
	v_mfma_f32_16x16x32_bf16 v[66:69], v[142:145], v[218:221], v[66:69]
	v_mfma_f32_16x16x32_bf16 v[130:133], v[150:153], v[182:185], v[94:97]
	v_mfma_f32_16x16x32_bf16 v[134:137], v[146:149], v[182:185], v[90:93]
	v_mfma_f32_16x16x32_bf16 v[86:89], v[150:153], v[210:213], v[86:89]
	v_mfma_f32_16x16x32_bf16 v[82:85], v[146:149], v[210:213], v[82:85]
	v_mfma_f32_16x16x32_bf16 v[78:81], v[150:153], v[222:225], v[78:81]
	v_mfma_f32_16x16x32_bf16 v[74:77], v[146:149], v[222:225], v[74:77]
	v_mfma_f32_16x16x32_bf16 v[70:73], v[150:153], v[226:229], v[70:73]
	v_mfma_f32_16x16x32_bf16 v[66:69], v[146:149], v[226:229], v[66:69]
	s_setprio 0
	s_barrier
	v_cndmask_b32_e64 v90, 0, 1, s[4:5]
	v_cmp_ne_u32_e64 s[6:7], 1, v90
	s_andn2_b64 vcc, exec, s[4:5]
	s_cbranch_vccnz .LBB0_371
	v_mov_b32_e32 v90, v0
	s_nop 0
	v_lshlrev_b32_e32 v91, 4, v90
	v_bitop3_b32 v91, v91, s3, v90 bitop3:0x48
	v_lshlrev_b32_e32 v90, 8, v90
	v_lshl_or_b32 v91, s55, 19, v91
	v_and_b32_e32 v90, 0xfffff800, v90
	v_add_u32_e32 v197, v91, v90
	v_add_u32_e32 v198, 0x40000, v197
	v_add_u32_e32 v199, 0x20000, v197
	v_add_u32_e32 v200, 0x60000, v197

.LBB0_560:
	s_mov_b32 s35, -2
	.p2align 3
	s_nop 0
	ds_read_b128 v[18:21], v179
	ds_read_b128 v[26:29], v179 offset:2048
	ds_read_b128 v[22:25], v180
	ds_read_b128 v[30:33], v180 offset:2048
	ds_read_b128 v[2:5], v181
	ds_read_b128 v[10:13], v181 offset:2048
	ds_read_b128 v[6:9], v182
	ds_read_b128 v[14:17], v182 offset:2048
	ds_read_b128 v[194:197], v183
	ds_read_b128 v[202:205], v183 offset:2048
	ds_read_b128 v[198:201], v184
	ds_read_b128 v[206:209], v184 offset:2048
	ds_read_b128 v[210:213], v183 offset:4096
	ds_read_b128 v[218:221], v183 offset:6144
	ds_read_b128 v[214:217], v184 offset:4096
	ds_read_b128 v[222:225], v184 offset:6144
	s_add_u32 s39, s18, s4
	s_addc_u32 s68, s19, s5
	s_add_u32 s42, s39, 0x80
	s_addc_u32 s43, s68, 0
	s_mov_b32 m0, s61
	s_nop 0
	global_load_lds_dwordx4 v172, s[42:43] offset:0
	s_nop 0
	s_mov_b32 m0, s62
	s_nop 0
	global_load_lds_dwordx4 v175, s[42:43] offset:0
	s_waitcnt vmcnt(8)
	s_waitcnt lgkmcnt(0)
	s_barrier
	s_setprio 1
	s_waitcnt lgkmcnt(5)
	v_mfma_f32_16x16x128_f8f6f4 v[158:161], v[18:25], v[194:201], 0
	v_mfma_f32_16x16x128_f8f6f4 v[150:153], v[26:33], v[194:201], 0
	s_waitcnt lgkmcnt(4)
	v_mfma_f32_16x16x128_f8f6f4 v[142:145], v[18:25], v[202:209], 0
	v_mfma_f32_16x16x128_f8f6f4 v[134:137], v[26:33], v[202:209], 0
	s_waitcnt lgkmcnt(1)
	v_mfma_f32_16x16x128_f8f6f4 v[126:129], v[18:25], v[210:217], 0
	v_mfma_f32_16x16x128_f8f6f4 v[118:121], v[26:33], v[210:217], 0
	s_waitcnt lgkmcnt(0)
	v_mfma_f32_16x16x128_f8f6f4 v[110:113], v[18:25], v[218:225], 0
	v_mfma_f32_16x16x128_f8f6f4 v[102:105], v[26:33], v[218:225], 0
	s_setprio 0
	s_setprio 1
	v_mfma_f32_16x16x128_f8f6f4 v[154:157], v[2:9], v[194:201], 0
	v_mfma_f32_16x16x128_f8f6f4 v[146:149], v[10:17], v[194:201], 0
	v_mfma_f32_16x16x128_f8f6f4 v[138:141], v[2:9], v[202:209], 0
	v_mfma_f32_16x16x128_f8f6f4 v[130:133], v[10:17], v[202:209], 0
	v_mfma_f32_16x16x128_f8f6f4 v[122:125], v[2:9], v[210:217], 0
	v_mfma_f32_16x16x128_f8f6f4 v[114:117], v[10:17], v[210:217], 0
	v_mfma_f32_16x16x128_f8f6f4 v[106:109], v[2:9], v[218:225], 0
	v_mfma_f32_16x16x128_f8f6f4 v[98:101], v[10:17], v[218:225], 0
	s_setprio 0
	s_barrier
	s_add_u32 s69, s44, s4
	s_addc_u32 s70, s45, s5
	ds_read_b128 v[194:197], v183 offset:16384
	ds_read_b128 v[202:205], v183 offset:18432
	ds_read_b128 v[198:201], v184 offset:16384
	ds_read_b128 v[206:209], v184 offset:18432
	ds_read_b128 v[210:213], v183 offset:20480
	ds_read_b128 v[218:221], v183 offset:22528
	ds_read_b128 v[214:217], v184 offset:20480
	ds_read_b128 v[222:225], v184 offset:22528
	s_add_u32 s42, s69, 0x100
	s_addc_u32 s43, s70, 0
	s_mov_b32 m0, s48
	s_nop 0
	global_load_lds_dwordx4 v1, s[42:43] offset:0
	s_nop 0
	s_mov_b32 m0, s49
	s_nop 0
	global_load_lds_dwordx4 v173, s[42:43] offset:0
	s_add_u32 s42, s69, 0x20100
	s_addc_u32 s43, s70, 0
	s_mov_b32 m0, s50
	s_nop 0
	global_load_lds_dwordx4 v1, s[42:43] offset:0
	s_nop 0
	s_mov_b32 m0, s51
	s_nop 0
	global_load_lds_dwordx4 v173, s[42:43] offset:0
	s_add_u32 s42, s39, 0x100
	s_addc_u32 s43, s68, 0
	s_mov_b32 m0, s29
	s_nop 0
	global_load_lds_dwordx4 v171, s[42:43] offset:0
	s_nop 0
	s_mov_b32 m0, s52
	s_nop 0
	global_load_lds_dwordx4 v174, s[42:43] offset:0
	s_waitcnt vmcnt(8)
	s_waitcnt lgkmcnt(0)
	s_barrier
	s_setprio 1
	s_waitcnt lgkmcnt(5)
	v_mfma_f32_16x16x128_f8f6f4 v[94:97], v[18:25], v[194:201], 0
	v_mfma_f32_16x16x128_f8f6f4 v[86:89], v[26:33], v[194:201], 0
	s_waitcnt lgkmcnt(4)
	v_mfma_f32_16x16x128_f8f6f4 v[78:81], v[18:25], v[202:209], 0
	v_mfma_f32_16x16x128_f8f6f4 v[70:73], v[26:33], v[202:209], 0
	s_waitcnt lgkmcnt(1)
	v_mfma_f32_16x16x128_f8f6f4 v[62:65], v[18:25], v[210:217], 0
	v_mfma_f32_16x16x128_f8f6f4 v[54:57], v[26:33], v[210:217], 0
	s_waitcnt lgkmcnt(0)
	v_mfma_f32_16x16x128_f8f6f4 v[46:49], v[18:25], v[218:225], 0
	v_mfma_f32_16x16x128_f8f6f4 v[38:41], v[26:33], v[218:225], 0
	s_setprio 0
	s_setprio 1
	v_mfma_f32_16x16x128_f8f6f4 v[90:93], v[2:9], v[194:201], 0
	v_mfma_f32_16x16x128_f8f6f4 v[82:85], v[10:17], v[194:201], 0
	v_mfma_f32_16x16x128_f8f6f4 v[74:77], v[2:9], v[202:209], 0
	v_mfma_f32_16x16x128_f8f6f4 v[66:69], v[10:17], v[202:209], 0
	v_mfma_f32_16x16x128_f8f6f4 v[58:61], v[2:9], v[210:217], 0
	v_mfma_f32_16x16x128_f8f6f4 v[50:53], v[10:17], v[210:217], 0
	v_mfma_f32_16x16x128_f8f6f4 v[42:45], v[2:9], v[218:225], 0
	v_mfma_f32_16x16x128_f8f6f4 v[34:37], v[10:17], v[218:225], 0
	s_setprio 0
	s_barrier
	s_add_i32 s71, 0, 0x18000
	v_add_u32_e32 v162, s71, v176
	v_add_u32_e32 v187, s71, v177
	s_add_i32 s71, 0, 0x1c000
	v_add_u32_e32 v194, s71, v176
	ds_read_b128 v[2:5], v162
	ds_read_b128 v[10:13], v162 offset:2048
	ds_read_b128 v[6:9], v187
	ds_read_b128 v[14:17], v187 offset:2048
	v_add_u32_e32 v195, s71, v177
	ds_read_b128 v[18:21], v194
	ds_read_b128 v[26:29], v194 offset:2048
	ds_read_b128 v[22:25], v195
	ds_read_b128 v[30:33], v195 offset:2048
	ds_read_b128 v[196:199], v183 offset:32768
	ds_read_b128 v[204:207], v183 offset:34816
	ds_read_b128 v[200:203], v184 offset:32768
	ds_read_b128 v[208:211], v184 offset:34816
	ds_read_b128 v[212:215], v183 offset:36864
	ds_read_b128 v[220:223], v183 offset:38912
	ds_read_b128 v[216:219], v184 offset:36864
	ds_read_b128 v[224:227], v184 offset:38912
	s_mov_b32 m0, s53
	s_nop 0
	global_load_lds_dwordx4 v172, s[42:43] offset:0
	s_nop 0
	s_mov_b32 m0, s54
	s_nop 0
	global_load_lds_dwordx4 v175, s[42:43] offset:0
	s_waitcnt vmcnt(8)
	s_waitcnt lgkmcnt(0)
	s_barrier
	s_setprio 1
	s_waitcnt lgkmcnt(5)
	v_mfma_f32_16x16x128_f8f6f4 v[158:161], v[2:9], v[196:203], v[158:161]
	v_mfma_f32_16x16x128_f8f6f4 v[150:153], v[10:17], v[196:203], v[150:153]
	s_waitcnt lgkmcnt(4)
	v_mfma_f32_16x16x128_f8f6f4 v[142:145], v[2:9], v[204:211], v[142:145]
	v_mfma_f32_16x16x128_f8f6f4 v[134:137], v[10:17], v[204:211], v[134:137]
	s_waitcnt lgkmcnt(1)
	v_mfma_f32_16x16x128_f8f6f4 v[126:129], v[2:9], v[212:219], v[126:129]
	v_mfma_f32_16x16x128_f8f6f4 v[118:121], v[10:17], v[212:219], v[118:121]
	s_waitcnt lgkmcnt(0)
	v_mfma_f32_16x16x128_f8f6f4 v[110:113], v[2:9], v[220:227], v[110:113]
	v_mfma_f32_16x16x128_f8f6f4 v[102:105], v[10:17], v[220:227], v[102:105]
	s_setprio 0
	s_setprio 1
	v_mfma_f32_16x16x128_f8f6f4 v[154:157], v[18:25], v[196:203], v[154:157]
	v_mfma_f32_16x16x128_f8f6f4 v[146:149], v[26:33], v[196:203], v[146:149]
	v_mfma_f32_16x16x128_f8f6f4 v[138:141], v[18:25], v[204:211], v[138:141]
	v_mfma_f32_16x16x128_f8f6f4 v[130:133], v[26:33], v[204:211], v[130:133]
	v_mfma_f32_16x16x128_f8f6f4 v[122:125], v[18:25], v[212:219], v[122:125]
	v_mfma_f32_16x16x128_f8f6f4 v[114:117], v[26:33], v[212:219], v[114:117]
	v_mfma_f32_16x16x128_f8f6f4 v[106:109], v[18:25], v[220:227], v[106:109]
	v_mfma_f32_16x16x128_f8f6f4 v[98:101], v[26:33], v[220:227], v[98:101]
	s_setprio 0
	s_barrier
	ds_read_b128 v[196:199], v183 offset:49152
	ds_read_b128 v[204:207], v183 offset:51200
	ds_read_b128 v[200:203], v184 offset:49152
	ds_read_b128 v[208:211], v184 offset:51200
	ds_read_b128 v[212:215], v183 offset:53248
	ds_read_b128 v[220:223], v183 offset:55296
	ds_read_b128 v[216:219], v184 offset:53248
	ds_read_b128 v[224:227], v184 offset:55296
	s_add_u32 s42, s69, 0x180
	s_addc_u32 s43, s70, 0
	s_mov_b32 m0, s55
	s_nop 0
	global_load_lds_dwordx4 v1, s[42:43] offset:0
	s_nop 0
	s_mov_b32 m0, s56
	s_nop 0
	global_load_lds_dwordx4 v173, s[42:43] offset:0
	s_add_u32 s42, s69, 0x20180
	s_addc_u32 s43, s70, 0
	s_mov_b32 m0, s59
	s_nop 0
	global_load_lds_dwordx4 v1, s[42:43] offset:0
	s_nop 0
	s_mov_b32 m0, s60
	s_nop 0
	global_load_lds_dwordx4 v173, s[42:43] offset:0
	s_add_u32 s42, s39, 0x180
	s_addc_u32 s43, s68, 0
	s_mov_b32 m0, s57
	s_nop 0
	global_load_lds_dwordx4 v171, s[42:43] offset:0
	s_nop 0
	s_mov_b32 m0, s58
	s_nop 0
	global_load_lds_dwordx4 v174, s[42:43] offset:0
	s_waitcnt vmcnt(8)
	s_waitcnt lgkmcnt(0)
	s_barrier
	s_setprio 1
	s_waitcnt lgkmcnt(5)
	v_mfma_f32_16x16x128_f8f6f4 v[94:97], v[2:9], v[196:203], v[94:97]
	v_mfma_f32_16x16x128_f8f6f4 v[86:89], v[10:17], v[196:203], v[86:89]
	s_waitcnt lgkmcnt(4)
	v_mfma_f32_16x16x128_f8f6f4 v[78:81], v[2:9], v[204:211], v[78:81]
	v_mfma_f32_16x16x128_f8f6f4 v[70:73], v[10:17], v[204:211], v[70:73]
	s_waitcnt lgkmcnt(1)
	v_mfma_f32_16x16x128_f8f6f4 v[62:65], v[2:9], v[212:219], v[62:65]
	v_mfma_f32_16x16x128_f8f6f4 v[54:57], v[10:17], v[212:219], v[54:57]
	s_waitcnt lgkmcnt(0)
	v_mfma_f32_16x16x128_f8f6f4 v[46:49], v[2:9], v[220:227], v[46:49]
	v_mfma_f32_16x16x128_f8f6f4 v[38:41], v[10:17], v[220:227], v[38:41]
	s_setprio 0
	s_setprio 1
	v_mfma_f32_16x16x128_f8f6f4 v[90:93], v[18:25], v[196:203], v[90:93]
	v_mfma_f32_16x16x128_f8f6f4 v[82:85], v[26:33], v[196:203], v[82:85]
	v_mfma_f32_16x16x128_f8f6f4 v[74:77], v[18:25], v[204:211], v[74:77]
	v_mfma_f32_16x16x128_f8f6f4 v[66:69], v[26:33], v[204:211], v[66:69]
	v_mfma_f32_16x16x128_f8f6f4 v[58:61], v[18:25], v[212:219], v[58:61]
	v_mfma_f32_16x16x128_f8f6f4 v[50:53], v[26:33], v[212:219], v[50:53]
	v_mfma_f32_16x16x128_f8f6f4 v[42:45], v[18:25], v[220:227], v[42:45]
	v_mfma_f32_16x16x128_f8f6f4 v[34:37], v[26:33], v[220:227], v[34:37]
	s_setprio 0
	s_add_i32 s35, s35, 2
	s_add_u32 s4, s4, 0x100
	s_addc_u32 s5, s5, 0
	s_barrier
.LBB0_561:
	.p2align 3
	s_nop 0
	ds_read_b128 v[18:21], v179
	ds_read_b128 v[26:29], v179 offset:2048
	ds_read_b128 v[22:25], v180
	ds_read_b128 v[30:33], v180 offset:2048
	ds_read_b128 v[2:5], v181
	ds_read_b128 v[10:13], v181 offset:2048
	ds_read_b128 v[6:9], v182
	ds_read_b128 v[14:17], v182 offset:2048
	ds_read_b128 v[194:197], v183
	ds_read_b128 v[202:205], v183 offset:2048
	ds_read_b128 v[198:201], v184
	ds_read_b128 v[206:209], v184 offset:2048
	ds_read_b128 v[210:213], v183 offset:4096
	ds_read_b128 v[218:221], v183 offset:6144
	ds_read_b128 v[214:217], v184 offset:4096
	ds_read_b128 v[222:225], v184 offset:6144
	s_add_u32 s39, s18, s4
	s_addc_u32 s68, s19, s5
	s_add_u32 s42, s39, 0x80
	s_addc_u32 s43, s68, 0
	s_mov_b32 m0, s61
	s_nop 0
	global_load_lds_dwordx4 v172, s[42:43] offset:0
	s_nop 0
	s_mov_b32 m0, s62
	s_nop 0
	global_load_lds_dwordx4 v175, s[42:43] offset:0
	s_waitcnt vmcnt(8)
	s_waitcnt lgkmcnt(0)
	s_barrier
	s_setprio 1
	s_waitcnt lgkmcnt(5)
	v_mfma_f32_16x16x128_f8f6f4 v[158:161], v[18:25], v[194:201], v[158:161]
	v_mfma_f32_16x16x128_f8f6f4 v[150:153], v[26:33], v[194:201], v[150:153]
	s_waitcnt lgkmcnt(4)
	v_mfma_f32_16x16x128_f8f6f4 v[142:145], v[18:25], v[202:209], v[142:145]
	v_mfma_f32_16x16x128_f8f6f4 v[134:137], v[26:33], v[202:209], v[134:137]
	s_waitcnt lgkmcnt(1)
	v_mfma_f32_16x16x128_f8f6f4 v[126:129], v[18:25], v[210:217], v[126:129]
	v_mfma_f32_16x16x128_f8f6f4 v[118:121], v[26:33], v[210:217], v[118:121]
	s_waitcnt lgkmcnt(0)
	v_mfma_f32_16x16x128_f8f6f4 v[110:113], v[18:25], v[218:225], v[110:113]
	v_mfma_f32_16x16x128_f8f6f4 v[102:105], v[26:33], v[218:225], v[102:105]
	s_setprio 0
	s_setprio 1
	v_mfma_f32_16x16x128_f8f6f4 v[154:157], v[2:9], v[194:201], v[154:157]
	v_mfma_f32_16x16x128_f8f6f4 v[146:149], v[10:17], v[194:201], v[146:149]
	v_mfma_f32_16x16x128_f8f6f4 v[138:141], v[2:9], v[202:209], v[138:141]
	v_mfma_f32_16x16x128_f8f6f4 v[130:133], v[10:17], v[202:209], v[130:133]
	v_mfma_f32_16x16x128_f8f6f4 v[122:125], v[2:9], v[210:217], v[122:125]
	v_mfma_f32_16x16x128_f8f6f4 v[114:117], v[10:17], v[210:217], v[114:117]
	v_mfma_f32_16x16x128_f8f6f4 v[106:109], v[2:9], v[218:225], v[106:109]
	v_mfma_f32_16x16x128_f8f6f4 v[98:101], v[10:17], v[218:225], v[98:101]
	s_setprio 0
	s_barrier
	s_add_u32 s69, s44, s4
	s_addc_u32 s70, s45, s5
	ds_read_b128 v[194:197], v183 offset:16384
	ds_read_b128 v[202:205], v183 offset:18432
	ds_read_b128 v[198:201], v184 offset:16384
	ds_read_b128 v[206:209], v184 offset:18432
	ds_read_b128 v[210:213], v183 offset:20480
	ds_read_b128 v[218:221], v183 offset:22528
	ds_read_b128 v[214:217], v184 offset:20480
	ds_read_b128 v[222:225], v184 offset:22528
	s_add_u32 s42, s69, 0x100
	s_addc_u32 s43, s70, 0
	s_mov_b32 m0, s48
	s_nop 0
	global_load_lds_dwordx4 v1, s[42:43] offset:0
	s_nop 0
	s_mov_b32 m0, s49
	s_nop 0
	global_load_lds_dwordx4 v173, s[42:43] offset:0
	s_add_u32 s42, s69, 0x20100
	s_addc_u32 s43, s70, 0
	s_mov_b32 m0, s50
	s_nop 0
	global_load_lds_dwordx4 v1, s[42:43] offset:0
	s_nop 0
	s_mov_b32 m0, s51
	s_nop 0
	global_load_lds_dwordx4 v173, s[42:43] offset:0
	s_add_u32 s42, s39, 0x100
	s_addc_u32 s43, s68, 0
	s_mov_b32 m0, s29
	s_nop 0
	global_load_lds_dwordx4 v171, s[42:43] offset:0
	s_nop 0
	s_mov_b32 m0, s52
	s_nop 0
	global_load_lds_dwordx4 v174, s[42:43] offset:0
	s_waitcnt vmcnt(8)
	s_waitcnt lgkmcnt(0)
	s_barrier
	s_setprio 1
	s_waitcnt lgkmcnt(5)
	v_mfma_f32_16x16x128_f8f6f4 v[94:97], v[18:25], v[194:201], v[94:97]
	v_mfma_f32_16x16x128_f8f6f4 v[86:89], v[26:33], v[194:201], v[86:89]
	s_waitcnt lgkmcnt(4)
	v_mfma_f32_16x16x128_f8f6f4 v[78:81], v[18:25], v[202:209], v[78:81]
	v_mfma_f32_16x16x128_f8f6f4 v[70:73], v[26:33], v[202:209], v[70:73]
	s_waitcnt lgkmcnt(1)
	v_mfma_f32_16x16x128_f8f6f4 v[62:65], v[18:25], v[210:217], v[62:65]
	v_mfma_f32_16x16x128_f8f6f4 v[54:57], v[26:33], v[210:217], v[54:57]
	s_waitcnt lgkmcnt(0)
	v_mfma_f32_16x16x128_f8f6f4 v[46:49], v[18:25], v[218:225], v[46:49]
	v_mfma_f32_16x16x128_f8f6f4 v[38:41], v[26:33], v[218:225], v[38:41]
	s_setprio 0
	s_setprio 1
	v_mfma_f32_16x16x128_f8f6f4 v[90:93], v[2:9], v[194:201], v[90:93]
	v_mfma_f32_16x16x128_f8f6f4 v[82:85], v[10:17], v[194:201], v[82:85]
	v_mfma_f32_16x16x128_f8f6f4 v[74:77], v[2:9], v[202:209], v[74:77]
	v_mfma_f32_16x16x128_f8f6f4 v[66:69], v[10:17], v[202:209], v[66:69]
	v_mfma_f32_16x16x128_f8f6f4 v[58:61], v[2:9], v[210:217], v[58:61]
	v_mfma_f32_16x16x128_f8f6f4 v[50:53], v[10:17], v[210:217], v[50:53]
	v_mfma_f32_16x16x128_f8f6f4 v[42:45], v[2:9], v[218:225], v[42:45]
	v_mfma_f32_16x16x128_f8f6f4 v[34:37], v[10:17], v[218:225], v[34:37]
	s_setprio 0
	s_barrier
	s_add_i32 s71, 0, 0x18000
	v_add_u32_e32 v162, s71, v176
	v_add_u32_e32 v187, s71, v177
	s_add_i32 s71, 0, 0x1c000
	v_add_u32_e32 v194, s71, v176
	ds_read_b128 v[2:5], v162
	ds_read_b128 v[10:13], v162 offset:2048
	ds_read_b128 v[6:9], v187
	ds_read_b128 v[14:17], v187 offset:2048
	v_add_u32_e32 v195, s71, v177
	ds_read_b128 v[18:21], v194
	ds_read_b128 v[26:29], v194 offset:2048
	ds_read_b128 v[22:25], v195
	ds_read_b128 v[30:33], v195 offset:2048
	ds_read_b128 v[196:199], v183 offset:32768
	ds_read_b128 v[204:207], v183 offset:34816
	ds_read_b128 v[200:203], v184 offset:32768
	ds_read_b128 v[208:211], v184 offset:34816
	ds_read_b128 v[212:215], v183 offset:36864
	ds_read_b128 v[220:223], v183 offset:38912
	ds_read_b128 v[216:219], v184 offset:36864
	ds_read_b128 v[224:227], v184 offset:38912
	s_mov_b32 m0, s53
	s_nop 0
	global_load_lds_dwordx4 v172, s[42:43] offset:0
	s_nop 0
	s_mov_b32 m0, s54
	s_nop 0
	global_load_lds_dwordx4 v175, s[42:43] offset:0
	s_waitcnt vmcnt(8)
	s_waitcnt lgkmcnt(0)
	s_barrier
	s_setprio 1
	s_waitcnt lgkmcnt(5)
	v_mfma_f32_16x16x128_f8f6f4 v[158:161], v[2:9], v[196:203], v[158:161]
	v_mfma_f32_16x16x128_f8f6f4 v[150:153], v[10:17], v[196:203], v[150:153]
	s_waitcnt lgkmcnt(4)
	v_mfma_f32_16x16x128_f8f6f4 v[142:145], v[2:9], v[204:211], v[142:145]
	v_mfma_f32_16x16x128_f8f6f4 v[134:137], v[10:17], v[204:211], v[134:137]
	s_waitcnt lgkmcnt(1)
	v_mfma_f32_16x16x128_f8f6f4 v[126:129], v[2:9], v[212:219], v[126:129]
	v_mfma_f32_16x16x128_f8f6f4 v[118:121], v[10:17], v[212:219], v[118:121]
	s_waitcnt lgkmcnt(0)
	v_mfma_f32_16x16x128_f8f6f4 v[110:113], v[2:9], v[220:227], v[110:113]
	v_mfma_f32_16x16x128_f8f6f4 v[102:105], v[10:17], v[220:227], v[102:105]
	s_setprio 0
	s_setprio 1
	v_mfma_f32_16x16x128_f8f6f4 v[154:157], v[18:25], v[196:203], v[154:157]
	v_mfma_f32_16x16x128_f8f6f4 v[146:149], v[26:33], v[196:203], v[146:149]
	v_mfma_f32_16x16x128_f8f6f4 v[138:141], v[18:25], v[204:211], v[138:141]
	v_mfma_f32_16x16x128_f8f6f4 v[130:133], v[26:33], v[204:211], v[130:133]
	v_mfma_f32_16x16x128_f8f6f4 v[122:125], v[18:25], v[212:219], v[122:125]
	v_mfma_f32_16x16x128_f8f6f4 v[114:117], v[26:33], v[212:219], v[114:117]
	v_mfma_f32_16x16x128_f8f6f4 v[106:109], v[18:25], v[220:227], v[106:109]
	v_mfma_f32_16x16x128_f8f6f4 v[98:101], v[26:33], v[220:227], v[98:101]
	s_setprio 0
	s_barrier
	ds_read_b128 v[196:199], v183 offset:49152
	ds_read_b128 v[204:207], v183 offset:51200
	ds_read_b128 v[200:203], v184 offset:49152
	ds_read_b128 v[208:211], v184 offset:51200
	ds_read_b128 v[212:215], v183 offset:53248
	ds_read_b128 v[220:223], v183 offset:55296
	ds_read_b128 v[216:219], v184 offset:53248
	ds_read_b128 v[224:227], v184 offset:55296
	s_add_u32 s42, s69, 0x180
	s_addc_u32 s43, s70, 0
	s_mov_b32 m0, s55
	s_nop 0
	global_load_lds_dwordx4 v1, s[42:43] offset:0
	s_nop 0
	s_mov_b32 m0, s56
	s_nop 0
	global_load_lds_dwordx4 v173, s[42:43] offset:0
	s_add_u32 s42, s69, 0x20180
	s_addc_u32 s43, s70, 0
	s_mov_b32 m0, s59
	s_nop 0
	global_load_lds_dwordx4 v1, s[42:43] offset:0
	s_nop 0
	s_mov_b32 m0, s60
	s_nop 0
	global_load_lds_dwordx4 v173, s[42:43] offset:0
	s_add_u32 s42, s39, 0x180
	s_addc_u32 s43, s68, 0
	s_mov_b32 m0, s57
	s_nop 0
	global_load_lds_dwordx4 v171, s[42:43] offset:0
	s_nop 0
	s_mov_b32 m0, s58
	s_nop 0
	global_load_lds_dwordx4 v174, s[42:43] offset:0
	s_waitcnt vmcnt(8)
	s_waitcnt lgkmcnt(0)
	s_barrier
	s_setprio 1
	s_waitcnt lgkmcnt(5)
	v_mfma_f32_16x16x128_f8f6f4 v[94:97], v[2:9], v[196:203], v[94:97]
	v_mfma_f32_16x16x128_f8f6f4 v[86:89], v[10:17], v[196:203], v[86:89]
	s_waitcnt lgkmcnt(4)
	v_mfma_f32_16x16x128_f8f6f4 v[78:81], v[2:9], v[204:211], v[78:81]
	v_mfma_f32_16x16x128_f8f6f4 v[70:73], v[10:17], v[204:211], v[70:73]
	s_waitcnt lgkmcnt(1)
	v_mfma_f32_16x16x128_f8f6f4 v[62:65], v[2:9], v[212:219], v[62:65]
	v_mfma_f32_16x16x128_f8f6f4 v[54:57], v[10:17], v[212:219], v[54:57]
	s_waitcnt lgkmcnt(0)
	v_mfma_f32_16x16x128_f8f6f4 v[46:49], v[2:9], v[220:227], v[46:49]
	v_mfma_f32_16x16x128_f8f6f4 v[38:41], v[10:17], v[220:227], v[38:41]
	s_setprio 0
	s_setprio 1
	v_mfma_f32_16x16x128_f8f6f4 v[90:93], v[18:25], v[196:203], v[90:93]
	v_mfma_f32_16x16x128_f8f6f4 v[82:85], v[26:33], v[196:203], v[82:85]
	v_mfma_f32_16x16x128_f8f6f4 v[74:77], v[18:25], v[204:211], v[74:77]
	v_mfma_f32_16x16x128_f8f6f4 v[66:69], v[26:33], v[204:211], v[66:69]
	v_mfma_f32_16x16x128_f8f6f4 v[58:61], v[18:25], v[212:219], v[58:61]
	v_mfma_f32_16x16x128_f8f6f4 v[50:53], v[26:33], v[212:219], v[50:53]
	v_mfma_f32_16x16x128_f8f6f4 v[42:45], v[18:25], v[220:227], v[42:45]
	v_mfma_f32_16x16x128_f8f6f4 v[34:37], v[26:33], v[220:227], v[34:37]
	s_setprio 0
	s_add_i32 s35, s35, 2
	s_add_u32 s4, s4, 0x100
	s_addc_u32 s5, s5, 0
	s_cmp_lt_u32 s35, 4
	s_barrier
	s_cbranch_scc1 .LBB0_561
	ds_read_b128 v[18:21], v179
	ds_read_b128 v[26:29], v179 offset:2048
	ds_read_b128 v[22:25], v180
	ds_read_b128 v[30:33], v180 offset:2048
	ds_read_b128 v[2:5], v181
	ds_read_b128 v[10:13], v181 offset:2048
	ds_read_b128 v[6:9], v182
	ds_read_b128 v[14:17], v182 offset:2048
	ds_read_b128 v[196:199], v183
	ds_read_b128 v[204:207], v183 offset:2048
	ds_read_b128 v[200:203], v184
	ds_read_b128 v[208:211], v184 offset:2048
	ds_read_b128 v[212:215], v183 offset:4096
	ds_read_b128 v[220:223], v183 offset:6144
	ds_read_b128 v[216:219], v184 offset:4096
	ds_read_b128 v[224:227], v184 offset:6144
	s_mov_b32 m0, s61
	s_nop 0
	global_load_lds_dwordx4 v172, s[24:25] offset:0
	s_nop 0
	s_mov_b32 m0, s62
	s_nop 0
	global_load_lds_dwordx4 v175, s[24:25] offset:0
	s_waitcnt vmcnt(8)
	s_waitcnt lgkmcnt(0)
	s_barrier
	s_setprio 1
	s_waitcnt lgkmcnt(5)
	v_mfma_f32_16x16x128_f8f6f4 v[158:161], v[18:25], v[196:203], v[158:161]
	v_mfma_f32_16x16x128_f8f6f4 v[150:153], v[26:33], v[196:203], v[150:153]
	s_waitcnt lgkmcnt(4)
	v_mfma_f32_16x16x128_f8f6f4 v[142:145], v[18:25], v[204:211], v[142:145]
	v_mfma_f32_16x16x128_f8f6f4 v[134:137], v[26:33], v[204:211], v[134:137]
	s_waitcnt lgkmcnt(1)
	v_mfma_f32_16x16x128_f8f6f4 v[126:129], v[18:25], v[212:219], v[126:129]
	v_mfma_f32_16x16x128_f8f6f4 v[118:121], v[26:33], v[212:219], v[118:121]
	s_waitcnt lgkmcnt(0)
	v_mfma_f32_16x16x128_f8f6f4 v[110:113], v[18:25], v[220:227], v[110:113]
	v_mfma_f32_16x16x128_f8f6f4 v[102:105], v[26:33], v[220:227], v[102:105]
	s_setprio 0
	s_setprio 1
	v_mfma_f32_16x16x128_f8f6f4 v[154:157], v[2:9], v[196:203], v[154:157]
	v_mfma_f32_16x16x128_f8f6f4 v[146:149], v[10:17], v[196:203], v[146:149]
	v_mfma_f32_16x16x128_f8f6f4 v[138:141], v[2:9], v[204:211], v[138:141]
	v_mfma_f32_16x16x128_f8f6f4 v[130:133], v[10:17], v[204:211], v[130:133]
	v_mfma_f32_16x16x128_f8f6f4 v[122:125], v[2:9], v[212:219], v[122:125]
	v_mfma_f32_16x16x128_f8f6f4 v[114:117], v[10:17], v[212:219], v[114:117]
	v_mfma_f32_16x16x128_f8f6f4 v[106:109], v[2:9], v[220:227], v[106:109]
	v_mfma_f32_16x16x128_f8f6f4 v[98:101], v[10:17], v[220:227], v[98:101]
	s_setprio 0
	s_barrier
	v_cndmask_b32_e64 v196, 0, 1, s[46:47]
	v_cmp_ne_u32_e64 s[4:5], 1, v196
	s_andn2_b64 vcc, exec, s[46:47]
	s_cbranch_vccnz .LBB0_564
	v_mov_b32_e32 v171, v0
	s_lshl_b32 s35, s66, 9
	s_add_i32 s35, s35, 0
	v_lshrrev_b32_e32 v172, 4, v171
	v_xor_b32_e32 v172, v172, v171
	s_add_i32 s35, s35, 0x20480
	v_ashrrev_i32_e32 v174, 3, v171
	v_lshl_add_u32 v171, v171, 4, v170
	v_lshl_add_u32 v174, v174, 1, s35
	v_ashrrev_i32_e32 v171, 7, v171
	v_lshl_add_u32 v171, v171, 1, s35
	ds_read_u16 v175, v174
	ds_read_u16 v174, v174 offset:256
	ds_read_u16 v196, v171
	ds_read_u16 v197, v171 offset:256
	v_lshlrev_b32_e32 v172, 4, v172
	v_and_b32_e32 v198, 0x70, v172
	s_waitcnt lgkmcnt(3)
	v_lshl_or_b32 v171, v175, 10, v198
	s_waitcnt lgkmcnt(2)
	v_lshl_or_b32 v172, v174, 10, v198
	s_waitcnt lgkmcnt(1)
	v_lshl_or_b32 v174, v196, 10, v198
	s_waitcnt lgkmcnt(0)
	v_lshl_or_b32 v175, v197, 10, v198

.LBB0_649:
	s_mov_b32 s35, -2
	.p2align 3
	s_nop 0
	ds_read_b128 v[18:21], v176
	ds_read_b128 v[26:29], v176 offset:2048
	ds_read_b128 v[22:25], v177
	ds_read_b128 v[30:33], v177 offset:2048
	ds_read_b128 v[2:5], v178
	ds_read_b128 v[10:13], v178 offset:2048
	ds_read_b128 v[6:9], v179
	ds_read_b128 v[14:17], v179 offset:2048
	ds_read_b128 v[194:197], v180
	ds_read_b128 v[202:205], v180 offset:2048
	ds_read_b128 v[198:201], v181
	ds_read_b128 v[206:209], v181 offset:2048
	ds_read_b128 v[210:213], v180 offset:4096
	ds_read_b128 v[218:221], v180 offset:6144
	ds_read_b128 v[214:217], v181 offset:4096
	ds_read_b128 v[222:225], v181 offset:6144
	s_add_u32 s64, s12, s4
	s_addc_u32 s65, s13, s5
	s_add_u32 s46, s64, 0x80
	s_addc_u32 s47, s65, 0
	s_mov_b32 m0, s58
	s_nop 0
	global_load_lds_dwordx4 v163, s[46:47] offset:0
	s_nop 0
	s_mov_b32 m0, s59
	s_nop 0
	global_load_lds_dwordx4 v171, s[46:47] offset:0
	s_waitcnt vmcnt(8)
	s_waitcnt lgkmcnt(0)
	s_barrier
	s_setprio 1
	s_waitcnt lgkmcnt(0)
	v_mfma_f32_16x16x128_f8f6f4 v[158:161], v[18:25], v[194:201], 0
	v_mfma_f32_16x16x128_f8f6f4 v[154:157], v[26:33], v[194:201], 0
	v_mfma_f32_16x16x128_f8f6f4 v[142:145], v[18:25], v[202:209], 0
	v_mfma_f32_16x16x128_f8f6f4 v[138:141], v[26:33], v[202:209], 0
	v_mfma_f32_16x16x128_f8f6f4 v[126:129], v[18:25], v[210:217], 0
	v_mfma_f32_16x16x128_f8f6f4 v[122:125], v[26:33], v[210:217], 0
	v_mfma_f32_16x16x128_f8f6f4 v[110:113], v[18:25], v[218:225], 0
	v_mfma_f32_16x16x128_f8f6f4 v[106:109], v[26:33], v[218:225], 0
	s_setprio 0
	s_setprio 1
	v_mfma_f32_16x16x128_f8f6f4 v[150:153], v[2:9], v[194:201], 0
	v_mfma_f32_16x16x128_f8f6f4 v[146:149], v[10:17], v[194:201], 0
	v_mfma_f32_16x16x128_f8f6f4 v[134:137], v[2:9], v[202:209], 0
	v_mfma_f32_16x16x128_f8f6f4 v[130:133], v[10:17], v[202:209], 0
	v_mfma_f32_16x16x128_f8f6f4 v[118:121], v[2:9], v[210:217], 0
	v_mfma_f32_16x16x128_f8f6f4 v[114:117], v[10:17], v[210:217], 0
	v_mfma_f32_16x16x128_f8f6f4 v[102:105], v[2:9], v[218:225], 0
	v_mfma_f32_16x16x128_f8f6f4 v[98:101], v[10:17], v[218:225], 0
	s_setprio 0
	s_barrier
	s_add_u32 s66, s42, s4
	s_addc_u32 s67, s43, s5
	ds_read_b128 v[194:197], v180 offset:16384
	ds_read_b128 v[202:205], v180 offset:18432
	ds_read_b128 v[198:201], v181 offset:16384
	ds_read_b128 v[206:209], v181 offset:18432
	ds_read_b128 v[210:213], v180 offset:20480
	ds_read_b128 v[218:221], v180 offset:22528
	ds_read_b128 v[214:217], v181 offset:20480
	ds_read_b128 v[222:225], v181 offset:22528
	s_add_u32 s46, s66, 0x100
	s_addc_u32 s47, s67, 0
	s_mov_b32 m0, s33
	s_nop 0
	global_load_lds_dwordx4 v172, s[46:47] offset:0
	s_nop 0
	s_mov_b32 m0, s39
	s_nop 0
	global_load_lds_dwordx4 v173, s[46:47] offset:0
	s_add_u32 s46, s66, 0x20100
	s_addc_u32 s47, s67, 0
	s_mov_b32 m0, s41
	s_nop 0
	global_load_lds_dwordx4 v172, s[46:47] offset:0
	s_nop 0
	s_mov_b32 m0, s48
	s_nop 0
	global_load_lds_dwordx4 v173, s[46:47] offset:0
	s_add_u32 s46, s64, 0x100
	s_addc_u32 s47, s65, 0
	s_mov_b32 m0, s1
	s_nop 0
	global_load_lds_dwordx4 v162, s[46:47] offset:0
	s_nop 0
	s_mov_b32 m0, s49
	s_nop 0
	global_load_lds_dwordx4 v170, s[46:47] offset:0
	s_waitcnt vmcnt(8)
	s_waitcnt lgkmcnt(0)
	s_barrier
	s_setprio 1
	s_waitcnt lgkmcnt(5)
	v_mfma_f32_16x16x128_f8f6f4 v[94:97], v[18:25], v[194:201], 0
	v_mfma_f32_16x16x128_f8f6f4 v[90:93], v[26:33], v[194:201], 0
	s_waitcnt lgkmcnt(4)
	v_mfma_f32_16x16x128_f8f6f4 v[78:81], v[18:25], v[202:209], 0
	v_mfma_f32_16x16x128_f8f6f4 v[74:77], v[26:33], v[202:209], 0
	s_waitcnt lgkmcnt(1)
	v_mfma_f32_16x16x128_f8f6f4 v[62:65], v[18:25], v[210:217], 0
	v_mfma_f32_16x16x128_f8f6f4 v[58:61], v[26:33], v[210:217], 0
	s_waitcnt lgkmcnt(0)
	v_mfma_f32_16x16x128_f8f6f4 v[46:49], v[18:25], v[218:225], 0
	v_mfma_f32_16x16x128_f8f6f4 v[42:45], v[26:33], v[218:225], 0
	s_setprio 0
	s_setprio 1
	v_mfma_f32_16x16x128_f8f6f4 v[86:89], v[2:9], v[194:201], 0
	v_mfma_f32_16x16x128_f8f6f4 v[82:85], v[10:17], v[194:201], 0
	v_mfma_f32_16x16x128_f8f6f4 v[70:73], v[2:9], v[202:209], 0
	v_mfma_f32_16x16x128_f8f6f4 v[66:69], v[10:17], v[202:209], 0
	v_mfma_f32_16x16x128_f8f6f4 v[54:57], v[2:9], v[210:217], 0
	v_mfma_f32_16x16x128_f8f6f4 v[50:53], v[10:17], v[210:217], 0
	v_mfma_f32_16x16x128_f8f6f4 v[38:41], v[2:9], v[218:225], 0
	v_mfma_f32_16x16x128_f8f6f4 v[34:37], v[10:17], v[218:225], 0
	s_setprio 0
	s_barrier
	s_add_i32 s68, 0, 0x18000
	v_add_u32_e32 v183, s68, v174
	v_add_u32_e32 v184, s68, v175
	s_add_i32 s68, 0, 0x1c000
	v_add_u32_e32 v185, s68, v174
	ds_read_b128 v[2:5], v183
	ds_read_b128 v[10:13], v183 offset:2048
	ds_read_b128 v[6:9], v184
	ds_read_b128 v[14:17], v184 offset:2048
	v_add_u32_e32 v186, s68, v175
	ds_read_b128 v[18:21], v185
	ds_read_b128 v[26:29], v185 offset:2048
	ds_read_b128 v[22:25], v186
	ds_read_b128 v[30:33], v186 offset:2048
	ds_read_b128 v[194:197], v180 offset:32768
	ds_read_b128 v[202:205], v180 offset:34816
	ds_read_b128 v[198:201], v181 offset:32768
	ds_read_b128 v[206:209], v181 offset:34816
	ds_read_b128 v[210:213], v180 offset:36864
	ds_read_b128 v[218:221], v180 offset:38912
	ds_read_b128 v[214:217], v181 offset:36864
	ds_read_b128 v[222:225], v181 offset:38912
	s_mov_b32 m0, s50
	s_nop 0
	global_load_lds_dwordx4 v163, s[46:47] offset:0
	s_nop 0
	s_mov_b32 m0, s51
	s_nop 0
	global_load_lds_dwordx4 v171, s[46:47] offset:0
	s_waitcnt vmcnt(8)
	s_waitcnt lgkmcnt(0)
	s_barrier
	s_setprio 1
	s_waitcnt lgkmcnt(5)
	v_mfma_f32_16x16x128_f8f6f4 v[158:161], v[2:9], v[194:201], v[158:161]
	v_mfma_f32_16x16x128_f8f6f4 v[154:157], v[10:17], v[194:201], v[154:157]
	s_waitcnt lgkmcnt(4)
	v_mfma_f32_16x16x128_f8f6f4 v[142:145], v[2:9], v[202:209], v[142:145]
	v_mfma_f32_16x16x128_f8f6f4 v[138:141], v[10:17], v[202:209], v[138:141]
	s_waitcnt lgkmcnt(1)
	v_mfma_f32_16x16x128_f8f6f4 v[126:129], v[2:9], v[210:217], v[126:129]
	v_mfma_f32_16x16x128_f8f6f4 v[122:125], v[10:17], v[210:217], v[122:125]
	s_waitcnt lgkmcnt(0)
	v_mfma_f32_16x16x128_f8f6f4 v[110:113], v[2:9], v[218:225], v[110:113]
	v_mfma_f32_16x16x128_f8f6f4 v[106:109], v[10:17], v[218:225], v[106:109]
	s_setprio 0
	s_setprio 1
	v_mfma_f32_16x16x128_f8f6f4 v[150:153], v[18:25], v[194:201], v[150:153]
	v_mfma_f32_16x16x128_f8f6f4 v[146:149], v[26:33], v[194:201], v[146:149]
	v_mfma_f32_16x16x128_f8f6f4 v[134:137], v[18:25], v[202:209], v[134:137]
	v_mfma_f32_16x16x128_f8f6f4 v[130:133], v[26:33], v[202:209], v[130:133]
	v_mfma_f32_16x16x128_f8f6f4 v[118:121], v[18:25], v[210:217], v[118:121]
	v_mfma_f32_16x16x128_f8f6f4 v[114:117], v[26:33], v[210:217], v[114:117]
	v_mfma_f32_16x16x128_f8f6f4 v[102:105], v[18:25], v[218:225], v[102:105]
	v_mfma_f32_16x16x128_f8f6f4 v[98:101], v[26:33], v[218:225], v[98:101]
	s_setprio 0
	s_barrier
	ds_read_b128 v[194:197], v180 offset:49152
	ds_read_b128 v[202:205], v180 offset:51200
	ds_read_b128 v[198:201], v181 offset:49152
	ds_read_b128 v[206:209], v181 offset:51200
	ds_read_b128 v[210:213], v180 offset:53248
	ds_read_b128 v[218:221], v180 offset:55296
	ds_read_b128 v[214:217], v181 offset:53248
	ds_read_b128 v[222:225], v181 offset:55296
	s_add_u32 s46, s66, 0x180
	s_addc_u32 s47, s67, 0
	s_mov_b32 m0, s52
	s_nop 0
	global_load_lds_dwordx4 v172, s[46:47] offset:0
	s_nop 0
	s_mov_b32 m0, s53
	s_nop 0
	global_load_lds_dwordx4 v173, s[46:47] offset:0
	s_add_u32 s46, s66, 0x20180
	s_addc_u32 s47, s67, 0
	s_mov_b32 m0, s56
	s_nop 0
	global_load_lds_dwordx4 v172, s[46:47] offset:0
	s_nop 0
	s_mov_b32 m0, s57
	s_nop 0
	global_load_lds_dwordx4 v173, s[46:47] offset:0
	s_add_u32 s46, s64, 0x180
	s_addc_u32 s47, s65, 0
	s_mov_b32 m0, s54
	s_nop 0
	global_load_lds_dwordx4 v162, s[46:47] offset:0
	s_nop 0
	s_mov_b32 m0, s55
	s_nop 0
	global_load_lds_dwordx4 v170, s[46:47] offset:0
	s_waitcnt vmcnt(8)
	s_waitcnt lgkmcnt(0)
	s_barrier
	s_setprio 1
	s_waitcnt lgkmcnt(5)
	v_mfma_f32_16x16x128_f8f6f4 v[94:97], v[2:9], v[194:201], v[94:97]
	v_mfma_f32_16x16x128_f8f6f4 v[90:93], v[10:17], v[194:201], v[90:93]
	s_waitcnt lgkmcnt(4)
	v_mfma_f32_16x16x128_f8f6f4 v[78:81], v[2:9], v[202:209], v[78:81]
	v_mfma_f32_16x16x128_f8f6f4 v[74:77], v[10:17], v[202:209], v[74:77]
	s_waitcnt lgkmcnt(1)
	v_mfma_f32_16x16x128_f8f6f4 v[62:65], v[2:9], v[210:217], v[62:65]
	v_mfma_f32_16x16x128_f8f6f4 v[58:61], v[10:17], v[210:217], v[58:61]
	s_waitcnt lgkmcnt(0)
	v_mfma_f32_16x16x128_f8f6f4 v[46:49], v[2:9], v[218:225], v[46:49]
	v_mfma_f32_16x16x128_f8f6f4 v[42:45], v[10:17], v[218:225], v[42:45]
	s_setprio 0
	s_setprio 1
	v_mfma_f32_16x16x128_f8f6f4 v[86:89], v[18:25], v[194:201], v[86:89]
	v_mfma_f32_16x16x128_f8f6f4 v[82:85], v[26:33], v[194:201], v[82:85]
	v_mfma_f32_16x16x128_f8f6f4 v[70:73], v[18:25], v[202:209], v[70:73]
	v_mfma_f32_16x16x128_f8f6f4 v[66:69], v[26:33], v[202:209], v[66:69]
	v_mfma_f32_16x16x128_f8f6f4 v[54:57], v[18:25], v[210:217], v[54:57]
	v_mfma_f32_16x16x128_f8f6f4 v[50:53], v[26:33], v[210:217], v[50:53]
	v_mfma_f32_16x16x128_f8f6f4 v[38:41], v[18:25], v[218:225], v[38:41]
	v_mfma_f32_16x16x128_f8f6f4 v[34:37], v[26:33], v[218:225], v[34:37]
	s_setprio 0
	s_add_i32 s35, s35, 2
	s_add_u32 s4, s4, 0x100
	s_addc_u32 s5, s5, 0
	s_barrier
.LBB0_650:
	.p2align 3
	s_nop 0
	ds_read_b128 v[18:21], v176
	ds_read_b128 v[26:29], v176 offset:2048
	ds_read_b128 v[22:25], v177
	ds_read_b128 v[30:33], v177 offset:2048
	ds_read_b128 v[2:5], v178
	ds_read_b128 v[10:13], v178 offset:2048
	ds_read_b128 v[6:9], v179
	ds_read_b128 v[14:17], v179 offset:2048
	ds_read_b128 v[194:197], v180
	ds_read_b128 v[202:205], v180 offset:2048
	ds_read_b128 v[198:201], v181
	ds_read_b128 v[206:209], v181 offset:2048
	ds_read_b128 v[210:213], v180 offset:4096
	ds_read_b128 v[218:221], v180 offset:6144
	ds_read_b128 v[214:217], v181 offset:4096
	ds_read_b128 v[222:225], v181 offset:6144
	s_add_u32 s64, s12, s4
	s_addc_u32 s65, s13, s5
	s_add_u32 s46, s64, 0x80
	s_addc_u32 s47, s65, 0
	s_mov_b32 m0, s58
	s_nop 0
	global_load_lds_dwordx4 v163, s[46:47] offset:0
	s_nop 0
	s_mov_b32 m0, s59
	s_nop 0
	global_load_lds_dwordx4 v171, s[46:47] offset:0
	s_waitcnt vmcnt(8)
	s_waitcnt lgkmcnt(0)
	s_barrier
	s_setprio 1
	s_waitcnt lgkmcnt(0)
	v_mfma_f32_16x16x128_f8f6f4 v[158:161], v[18:25], v[194:201], v[158:161]
	v_mfma_f32_16x16x128_f8f6f4 v[154:157], v[26:33], v[194:201], v[154:157]
	v_mfma_f32_16x16x128_f8f6f4 v[142:145], v[18:25], v[202:209], v[142:145]
	v_mfma_f32_16x16x128_f8f6f4 v[138:141], v[26:33], v[202:209], v[138:141]
	v_mfma_f32_16x16x128_f8f6f4 v[126:129], v[18:25], v[210:217], v[126:129]
	v_mfma_f32_16x16x128_f8f6f4 v[122:125], v[26:33], v[210:217], v[122:125]
	v_mfma_f32_16x16x128_f8f6f4 v[110:113], v[18:25], v[218:225], v[110:113]
	v_mfma_f32_16x16x128_f8f6f4 v[106:109], v[26:33], v[218:225], v[106:109]
	s_setprio 0
	s_setprio 1
	v_mfma_f32_16x16x128_f8f6f4 v[150:153], v[2:9], v[194:201], v[150:153]
	v_mfma_f32_16x16x128_f8f6f4 v[146:149], v[10:17], v[194:201], v[146:149]
	v_mfma_f32_16x16x128_f8f6f4 v[134:137], v[2:9], v[202:209], v[134:137]
	v_mfma_f32_16x16x128_f8f6f4 v[130:133], v[10:17], v[202:209], v[130:133]
	v_mfma_f32_16x16x128_f8f6f4 v[118:121], v[2:9], v[210:217], v[118:121]
	v_mfma_f32_16x16x128_f8f6f4 v[114:117], v[10:17], v[210:217], v[114:117]
	v_mfma_f32_16x16x128_f8f6f4 v[102:105], v[2:9], v[218:225], v[102:105]
	v_mfma_f32_16x16x128_f8f6f4 v[98:101], v[10:17], v[218:225], v[98:101]
	s_setprio 0
	s_barrier
	s_add_u32 s66, s42, s4
	s_addc_u32 s67, s43, s5
	ds_read_b128 v[194:197], v180 offset:16384
	ds_read_b128 v[202:205], v180 offset:18432
	ds_read_b128 v[198:201], v181 offset:16384
	ds_read_b128 v[206:209], v181 offset:18432
	ds_read_b128 v[210:213], v180 offset:20480
	ds_read_b128 v[218:221], v180 offset:22528
	ds_read_b128 v[214:217], v181 offset:20480
	ds_read_b128 v[222:225], v181 offset:22528
	s_add_u32 s46, s66, 0x100
	s_addc_u32 s47, s67, 0
	s_mov_b32 m0, s33
	s_nop 0
	global_load_lds_dwordx4 v172, s[46:47] offset:0
	s_nop 0
	s_mov_b32 m0, s39
	s_nop 0
	global_load_lds_dwordx4 v173, s[46:47] offset:0
	s_add_u32 s46, s66, 0x20100
	s_addc_u32 s47, s67, 0
	s_mov_b32 m0, s41
	s_nop 0
	global_load_lds_dwordx4 v172, s[46:47] offset:0
	s_nop 0
	s_mov_b32 m0, s48
	s_nop 0
	global_load_lds_dwordx4 v173, s[46:47] offset:0
	s_add_u32 s46, s64, 0x100
	s_addc_u32 s47, s65, 0
	s_mov_b32 m0, s1
	s_nop 0
	global_load_lds_dwordx4 v162, s[46:47] offset:0
	s_nop 0
	s_mov_b32 m0, s49
	s_nop 0
	global_load_lds_dwordx4 v170, s[46:47] offset:0
	s_waitcnt vmcnt(8)
	s_waitcnt lgkmcnt(0)
	s_barrier
	s_setprio 1
	s_waitcnt lgkmcnt(5)
	v_mfma_f32_16x16x128_f8f6f4 v[94:97], v[18:25], v[194:201], v[94:97]
	v_mfma_f32_16x16x128_f8f6f4 v[90:93], v[26:33], v[194:201], v[90:93]
	s_waitcnt lgkmcnt(4)
	v_mfma_f32_16x16x128_f8f6f4 v[78:81], v[18:25], v[202:209], v[78:81]
	v_mfma_f32_16x16x128_f8f6f4 v[74:77], v[26:33], v[202:209], v[74:77]
	s_waitcnt lgkmcnt(1)
	v_mfma_f32_16x16x128_f8f6f4 v[62:65], v[18:25], v[210:217], v[62:65]
	v_mfma_f32_16x16x128_f8f6f4 v[58:61], v[26:33], v[210:217], v[58:61]
	s_waitcnt lgkmcnt(0)
	v_mfma_f32_16x16x128_f8f6f4 v[46:49], v[18:25], v[218:225], v[46:49]
	v_mfma_f32_16x16x128_f8f6f4 v[42:45], v[26:33], v[218:225], v[42:45]
	s_setprio 0
	s_setprio 1
	v_mfma_f32_16x16x128_f8f6f4 v[86:89], v[2:9], v[194:201], v[86:89]
	v_mfma_f32_16x16x128_f8f6f4 v[82:85], v[10:17], v[194:201], v[82:85]
	v_mfma_f32_16x16x128_f8f6f4 v[70:73], v[2:9], v[202:209], v[70:73]
	v_mfma_f32_16x16x128_f8f6f4 v[66:69], v[10:17], v[202:209], v[66:69]
	v_mfma_f32_16x16x128_f8f6f4 v[54:57], v[2:9], v[210:217], v[54:57]
	v_mfma_f32_16x16x128_f8f6f4 v[50:53], v[10:17], v[210:217], v[50:53]
	v_mfma_f32_16x16x128_f8f6f4 v[38:41], v[2:9], v[218:225], v[38:41]
	v_mfma_f32_16x16x128_f8f6f4 v[34:37], v[10:17], v[218:225], v[34:37]
	s_setprio 0
	s_barrier
	s_add_i32 s68, 0, 0x18000
	v_add_u32_e32 v183, s68, v174
	v_add_u32_e32 v184, s68, v175
	s_add_i32 s68, 0, 0x1c000
	v_add_u32_e32 v185, s68, v174
	ds_read_b128 v[2:5], v183
	ds_read_b128 v[10:13], v183 offset:2048
	ds_read_b128 v[6:9], v184
	ds_read_b128 v[14:17], v184 offset:2048
	v_add_u32_e32 v186, s68, v175
	ds_read_b128 v[18:21], v185
	ds_read_b128 v[26:29], v185 offset:2048
	ds_read_b128 v[22:25], v186
	ds_read_b128 v[30:33], v186 offset:2048
	ds_read_b128 v[194:197], v180 offset:32768
	ds_read_b128 v[202:205], v180 offset:34816
	ds_read_b128 v[198:201], v181 offset:32768
	ds_read_b128 v[206:209], v181 offset:34816
	ds_read_b128 v[210:213], v180 offset:36864
	ds_read_b128 v[218:221], v180 offset:38912
	ds_read_b128 v[214:217], v181 offset:36864
	ds_read_b128 v[222:225], v181 offset:38912
	s_mov_b32 m0, s50
	s_nop 0
	global_load_lds_dwordx4 v163, s[46:47] offset:0
	s_nop 0
	s_mov_b32 m0, s51
	s_nop 0
	global_load_lds_dwordx4 v171, s[46:47] offset:0
	s_waitcnt vmcnt(8)
	s_waitcnt lgkmcnt(0)
	s_barrier
	s_setprio 1
	s_waitcnt lgkmcnt(5)
	v_mfma_f32_16x16x128_f8f6f4 v[158:161], v[2:9], v[194:201], v[158:161]
	v_mfma_f32_16x16x128_f8f6f4 v[154:157], v[10:17], v[194:201], v[154:157]
	s_waitcnt lgkmcnt(4)
	v_mfma_f32_16x16x128_f8f6f4 v[142:145], v[2:9], v[202:209], v[142:145]
	v_mfma_f32_16x16x128_f8f6f4 v[138:141], v[10:17], v[202:209], v[138:141]
	s_waitcnt lgkmcnt(1)
	v_mfma_f32_16x16x128_f8f6f4 v[126:129], v[2:9], v[210:217], v[126:129]
	v_mfma_f32_16x16x128_f8f6f4 v[122:125], v[10:17], v[210:217], v[122:125]
	s_waitcnt lgkmcnt(0)
	v_mfma_f32_16x16x128_f8f6f4 v[110:113], v[2:9], v[218:225], v[110:113]
	v_mfma_f32_16x16x128_f8f6f4 v[106:109], v[10:17], v[218:225], v[106:109]
	s_setprio 0
	s_setprio 1
	v_mfma_f32_16x16x128_f8f6f4 v[150:153], v[18:25], v[194:201], v[150:153]
	v_mfma_f32_16x16x128_f8f6f4 v[146:149], v[26:33], v[194:201], v[146:149]
	v_mfma_f32_16x16x128_f8f6f4 v[134:137], v[18:25], v[202:209], v[134:137]
	v_mfma_f32_16x16x128_f8f6f4 v[130:133], v[26:33], v[202:209], v[130:133]
	v_mfma_f32_16x16x128_f8f6f4 v[118:121], v[18:25], v[210:217], v[118:121]
	v_mfma_f32_16x16x128_f8f6f4 v[114:117], v[26:33], v[210:217], v[114:117]
	v_mfma_f32_16x16x128_f8f6f4 v[102:105], v[18:25], v[218:225], v[102:105]
	v_mfma_f32_16x16x128_f8f6f4 v[98:101], v[26:33], v[218:225], v[98:101]
	s_setprio 0
	s_barrier
	ds_read_b128 v[194:197], v180 offset:49152
	ds_read_b128 v[202:205], v180 offset:51200
	ds_read_b128 v[198:201], v181 offset:49152
	ds_read_b128 v[206:209], v181 offset:51200
	ds_read_b128 v[210:213], v180 offset:53248
	ds_read_b128 v[218:221], v180 offset:55296
	ds_read_b128 v[214:217], v181 offset:53248
	ds_read_b128 v[222:225], v181 offset:55296
	s_add_u32 s46, s66, 0x180
	s_addc_u32 s47, s67, 0
	s_mov_b32 m0, s52
	s_nop 0
	global_load_lds_dwordx4 v172, s[46:47] offset:0
	s_nop 0
	s_mov_b32 m0, s53
	s_nop 0
	global_load_lds_dwordx4 v173, s[46:47] offset:0
	s_add_u32 s46, s66, 0x20180
	s_addc_u32 s47, s67, 0
	s_mov_b32 m0, s56
	s_nop 0
	global_load_lds_dwordx4 v172, s[46:47] offset:0
	s_nop 0
	s_mov_b32 m0, s57
	s_nop 0
	global_load_lds_dwordx4 v173, s[46:47] offset:0
	s_add_u32 s46, s64, 0x180
	s_addc_u32 s47, s65, 0
	s_mov_b32 m0, s54
	s_nop 0
	global_load_lds_dwordx4 v162, s[46:47] offset:0
	s_nop 0
	s_mov_b32 m0, s55
	s_nop 0
	global_load_lds_dwordx4 v170, s[46:47] offset:0
	s_waitcnt vmcnt(8)
	s_waitcnt lgkmcnt(0)
	s_barrier
	s_setprio 1
	s_waitcnt lgkmcnt(5)
	v_mfma_f32_16x16x128_f8f6f4 v[94:97], v[2:9], v[194:201], v[94:97]
	v_mfma_f32_16x16x128_f8f6f4 v[90:93], v[10:17], v[194:201], v[90:93]
	s_waitcnt lgkmcnt(4)
	v_mfma_f32_16x16x128_f8f6f4 v[78:81], v[2:9], v[202:209], v[78:81]
	v_mfma_f32_16x16x128_f8f6f4 v[74:77], v[10:17], v[202:209], v[74:77]
	s_waitcnt lgkmcnt(1)
	v_mfma_f32_16x16x128_f8f6f4 v[62:65], v[2:9], v[210:217], v[62:65]
	v_mfma_f32_16x16x128_f8f6f4 v[58:61], v[10:17], v[210:217], v[58:61]
	s_waitcnt lgkmcnt(0)
	v_mfma_f32_16x16x128_f8f6f4 v[46:49], v[2:9], v[218:225], v[46:49]
	v_mfma_f32_16x16x128_f8f6f4 v[42:45], v[10:17], v[218:225], v[42:45]
	s_setprio 0
	s_setprio 1
	v_mfma_f32_16x16x128_f8f6f4 v[86:89], v[18:25], v[194:201], v[86:89]
	v_mfma_f32_16x16x128_f8f6f4 v[82:85], v[26:33], v[194:201], v[82:85]
	v_mfma_f32_16x16x128_f8f6f4 v[70:73], v[18:25], v[202:209], v[70:73]
	v_mfma_f32_16x16x128_f8f6f4 v[66:69], v[26:33], v[202:209], v[66:69]
	v_mfma_f32_16x16x128_f8f6f4 v[54:57], v[18:25], v[210:217], v[54:57]
	v_mfma_f32_16x16x128_f8f6f4 v[50:53], v[26:33], v[210:217], v[50:53]
	v_mfma_f32_16x16x128_f8f6f4 v[38:41], v[18:25], v[218:225], v[38:41]
	v_mfma_f32_16x16x128_f8f6f4 v[34:37], v[26:33], v[218:225], v[34:37]
	s_setprio 0
	s_add_i32 s35, s35, 2
	s_add_u32 s4, s4, 0x100
	s_addc_u32 s5, s5, 0
	s_cmp_lt_u32 s35, 4
	s_barrier
	s_cbranch_scc1 .LBB0_650
	ds_read_b128 v[18:21], v176
	ds_read_b128 v[26:29], v176 offset:2048
	ds_read_b128 v[22:25], v177
	ds_read_b128 v[30:33], v177 offset:2048
	ds_read_b128 v[2:5], v178
	ds_read_b128 v[10:13], v178 offset:2048
	ds_read_b128 v[6:9], v179
	ds_read_b128 v[14:17], v179 offset:2048
	ds_read_b128 v[194:197], v180
	ds_read_b128 v[202:205], v180 offset:2048
	ds_read_b128 v[198:201], v181
	ds_read_b128 v[206:209], v181 offset:2048
	ds_read_b128 v[210:213], v180 offset:4096
	ds_read_b128 v[218:221], v180 offset:6144
	ds_read_b128 v[214:217], v181 offset:4096
	ds_read_b128 v[222:225], v181 offset:6144
	s_mov_b32 m0, s58
	s_nop 0
	global_load_lds_dwordx4 v163, s[24:25] offset:0
	s_nop 0
	s_mov_b32 m0, s59
	s_nop 0
	global_load_lds_dwordx4 v171, s[24:25] offset:0
	s_waitcnt vmcnt(8)
	s_waitcnt lgkmcnt(0)
	s_barrier
	s_setprio 1
	s_waitcnt lgkmcnt(5)
	v_mfma_f32_16x16x128_f8f6f4 v[158:161], v[18:25], v[194:201], v[158:161]
	v_mfma_f32_16x16x128_f8f6f4 v[154:157], v[26:33], v[194:201], v[154:157]
	s_waitcnt lgkmcnt(4)
	v_mfma_f32_16x16x128_f8f6f4 v[142:145], v[18:25], v[202:209], v[142:145]
	v_mfma_f32_16x16x128_f8f6f4 v[138:141], v[26:33], v[202:209], v[138:141]
	s_waitcnt lgkmcnt(1)
	v_mfma_f32_16x16x128_f8f6f4 v[126:129], v[18:25], v[210:217], v[126:129]
	v_mfma_f32_16x16x128_f8f6f4 v[122:125], v[26:33], v[210:217], v[122:125]
	s_waitcnt lgkmcnt(0)
	v_mfma_f32_16x16x128_f8f6f4 v[110:113], v[18:25], v[218:225], v[110:113]
	v_mfma_f32_16x16x128_f8f6f4 v[106:109], v[26:33], v[218:225], v[106:109]
	s_setprio 0
	s_setprio 1
	v_mfma_f32_16x16x128_f8f6f4 v[150:153], v[2:9], v[194:201], v[150:153]
	v_mfma_f32_16x16x128_f8f6f4 v[146:149], v[10:17], v[194:201], v[146:149]
	v_mfma_f32_16x16x128_f8f6f4 v[134:137], v[2:9], v[202:209], v[134:137]
	v_mfma_f32_16x16x128_f8f6f4 v[130:133], v[10:17], v[202:209], v[130:133]
	v_mfma_f32_16x16x128_f8f6f4 v[118:121], v[2:9], v[210:217], v[118:121]
	v_mfma_f32_16x16x128_f8f6f4 v[114:117], v[10:17], v[210:217], v[114:117]
	v_mfma_f32_16x16x128_f8f6f4 v[102:105], v[2:9], v[218:225], v[102:105]
	v_mfma_f32_16x16x128_f8f6f4 v[98:101], v[10:17], v[218:225], v[98:101]
	s_setprio 0
	s_barrier
	v_cndmask_b32_e64 v187, 0, 1, s[44:45]
	v_cmp_ne_u32_e64 s[4:5], 1, v187
	s_andn2_b64 vcc, exec, s[44:45]
	s_cbranch_vccnz .LBB0_653
	v_mov_b32_e32 v162, v0
	s_nop 0
	v_lshlrev_b32_e32 v163, 4, v162
	v_bitop3_b32 v163, v163, s0, v162 bitop3:0x48
	v_lshlrev_b32_e32 v162, 7, v162
	v_lshl_or_b32 v163, s61, 18, v163
	v_and_b32_e32 v162, 0xfffffc00, v162
	v_add_u32_e32 v162, v163, v162
	v_add_u32_e32 v163, 0x20000, v162
	v_add_u32_e32 v170, 0x10000, v162
	v_add_u32_e32 v171, 0x30000, v162
